# retention out pass output loop software-pipelined: gate loads two iterations ahead and issued before the stores (counted vmcnt), LDS row read one iteration ahead
# speedup vs baseline: 1.0072x; 1.0032x over previous
; #define LAS __attribute__((address_space(3)))
; __device__ __forceinline__ bf16_t f2bf(float f) { unsigned u = __builtin_bit_cast(unsigned, f); return (bf16_t)((u + 0x7fffu + ((u >> 16) & 1u)) >> 16); }
; __device__ __forceinline__ int crow(int r, int hi) { return (r & 3) + 8 * (r >> 2) + 4 * hi; }
; __device__ __forceinline__ int crow(int r, int hi) { return (r & 3) + 8 * (r >> 2) + 4 * hi; }
; template <int DK, int DV, bool MLSTM>
; __device__ __forceinline__ void out_unit2(LAS unsigned char* lds, LAS unsigned char* ldstab, const OutArgs a, const int wv) {
;     ...
;     __syncthreads();
;     constexpr int TP = DV * 2;
;     static_assert(128 * TP <= 2 * NPK * 32768, "output tile fits the Q + K regions");
; #pragma unroll
;     for (int r = 0; r < 16; ++r) {
;         const int row = 32 * rb + crow(r, hi);
;         const float t1 = s1[r] + exch[((1 - dh) * 128 + row) * 2], t2 = s2[r] + exch[((1 - dh) * 128 + row) * 2 + 1];
;         float mean, inv;
;         if (MLSTM) { mean = 0.f; inv = rsqrtf(t2 * (1.f / DV) + EPS); }
;         else { mean = t1 * (1.f / DV); inv = rsqrtf(fmaxf(t2 * (1.f / DV) - mean * mean, 0.f) + EPS); }
; #pragma unroll
;         for (int nb = 0; nb < NB; ++nb) { const int col = dh * (DV / 2) + 32 * nb + r32;
;             *(LAS bf16_t*)(lds + row * TP + col * 2) = f2bf((o[nb][r] - mean) * inv); }
.LBB0_1838:
	s_or_b64 exec, exec, s[4:5]
	v_lshlrev_b32_e32 v164, 1, v219
	v_subrev_u32_e32 v164, s6, v164
	s_add_i32 s4, 0, 0x22100
	v_lshl_add_u32 v164, v164, 2, s4
	s_waitcnt vmcnt(0) lgkmcnt(0)
	s_barrier
	ds_read_b128 v[164:167], v164 offset:1024
	v_lshlrev_b32_e32 v168, 1, v217
	v_subrev_u32_e32 v168, s6, v168
	v_lshl_add_u32 v168, v168, 2, s4
	ds_read2_b64 v[168:171], v168 offset0:128 offset1:129
	s_waitcnt lgkmcnt(1)
	v_pk_add_f32 v[156:157], v[156:157], v[164:165]
	s_nop 0
	v_pk_mul_f32 v[156:157], v[156:157], s[36:37] op_sel_hi:[1,0]
	s_nop 0
	v_fma_f32 v157, -v156, v156, v157
	v_max_f32_e32 v157, 0, v157
	v_add_f32_e32 v157, 0x358637bd, v157
	v_mul_f32_e32 v164, 0x4b800000, v157
	v_cmp_gt_f32_e32 vcc, s89, v157
	v_sub_f32_e32 v16, v16, v156
	v_sub_f32_e32 v0, v0, v156
	v_cndmask_b32_e32 v157, v157, v164, vcc
	v_rsq_f32_e32 v157, v157
	v_or_b32_e32 v164, s6, v233
	v_mul_f32_e32 v165, 0x45800000, v157
	v_cndmask_b32_e32 v157, v157, v165, vcc
	v_mul_f32_e32 v16, v16, v157
	v_bfe_u32 v172, v16, 16, 1
	v_lshlrev_b32_e32 v165, 10, v219
	v_add3_u32 v172, v16, v172, s90
	v_lshlrev_b32_e32 v16, 1, v164
	v_mul_f32_e32 v0, v0, v157
	v_add3_u32 v164, 0, v165, v16
	v_bfe_u32 v165, v0, 16, 1
	v_add3_u32 v0, v0, v165, s90
	ds_write_b16_d16_hi v164, v0 offset:64
	v_sub_f32_e32 v0, v32, v156
	v_mul_f32_e32 v0, v0, v157
	v_bfe_u32 v32, v0, 16, 1
	v_add3_u32 v0, v0, v32, s90
	ds_write_b16_d16_hi v164, v0 offset:128
	v_sub_f32_e32 v0, v48, v156
	v_mul_f32_e32 v0, v0, v157
	v_bfe_u32 v32, v0, 16, 1
	v_add3_u32 v0, v0, v32, s90
	ds_write_b16_d16_hi v164, v0 offset:192
	v_sub_f32_e32 v0, v96, v156
	v_mul_f32_e32 v0, v0, v157
	v_bfe_u32 v32, v0, 16, 1
	v_add3_u32 v0, v0, v32, s90
	ds_write_b16_d16_hi v164, v0 offset:256
	v_sub_f32_e32 v0, v112, v156
	v_mul_f32_e32 v0, v0, v157
	v_bfe_u32 v32, v0, 16, 1
	v_add3_u32 v0, v0, v32, s90
	ds_write_b16_d16_hi v164, v0 offset:320
	v_sub_f32_e32 v0, v80, v156
	v_mul_f32_e32 v0, v0, v157
	v_bfe_u32 v32, v0, 16, 1
	v_add3_u32 v0, v0, v32, s90
	ds_write_b16_d16_hi v164, v0 offset:384
	v_sub_f32_e32 v0, v64, v156
	v_mul_f32_e32 v0, v0, v157
	v_pk_add_f32 v[156:157], v[158:159], v[166:167]
	ds_write_b16_d16_hi v164, v172
	v_pk_mul_f32 v[156:157], v[156:157], s[36:37] op_sel_hi:[1,0]
	s_nop 0
	v_fma_f32 v32, -v156, v156, v157
	v_max_f32_e32 v32, 0, v32
	v_add_f32_e32 v32, 0x358637bd, v32
	v_mul_f32_e32 v48, 0x4b800000, v32
	v_cmp_gt_f32_e32 vcc, s89, v32
	v_sub_f32_e32 v17, v17, v156
	v_sub_f32_e32 v1, v1, v156
	v_cndmask_b32_e32 v32, v32, v48, vcc
	v_rsq_f32_e32 v32, v32
	v_bfe_u32 v48, v0, 16, 1
	v_add3_u32 v0, v0, v48, s90
	ds_write_b16_d16_hi v164, v0 offset:448
	v_mul_f32_e32 v0, 0x45800000, v32
	v_cndmask_b32_e32 v0, v32, v0, vcc
	v_mul_f32_e32 v17, v17, v0
	v_lshlrev_b32_e32 v32, 10, v218
	v_bfe_u32 v48, v17, 16, 1
	v_add3_u32 v17, v17, v48, s90
	v_add3_u32 v32, 0, v32, v16
	v_mul_f32_e32 v1, v1, v0
	ds_write_b16_d16_hi v32, v17
	v_bfe_u32 v17, v1, 16, 1
	v_add3_u32 v1, v1, v17, s90
	ds_write_b16_d16_hi v32, v1 offset:64
	v_sub_f32_e32 v1, v33, v156
	v_mul_f32_e32 v1, v1, v0
	v_bfe_u32 v17, v1, 16, 1
	v_add3_u32 v1, v1, v17, s90
	ds_write_b16_d16_hi v32, v1 offset:128
	v_sub_f32_e32 v1, v49, v156
	v_mul_f32_e32 v1, v1, v0
	v_bfe_u32 v17, v1, 16, 1
	v_add3_u32 v1, v1, v17, s90
	ds_write_b16_d16_hi v32, v1 offset:192
	v_sub_f32_e32 v1, v97, v156
	v_mul_f32_e32 v1, v1, v0
	v_bfe_u32 v17, v1, 16, 1
	v_add3_u32 v1, v1, v17, s90
	ds_write_b16_d16_hi v32, v1 offset:256
	v_sub_f32_e32 v1, v113, v156
	v_mul_f32_e32 v1, v1, v0
	v_bfe_u32 v17, v1, 16, 1
	v_add3_u32 v1, v1, v17, s90
	ds_write_b16_d16_hi v32, v1 offset:320
	v_sub_f32_e32 v1, v81, v156
	v_mul_f32_e32 v1, v1, v0
	v_bfe_u32 v17, v1, 16, 1
	v_add3_u32 v1, v1, v17, s90
	ds_write_b16_d16_hi v32, v1 offset:384
	v_sub_f32_e32 v1, v65, v156
	v_mul_f32_e32 v17, v1, v0
	s_waitcnt lgkmcnt(14)
	v_pk_add_f32 v[0:1], v[152:153], v[168:169]
	s_nop 0
	v_pk_mul_f32 v[0:1], v[0:1], s[36:37] op_sel_hi:[1,0]
	s_nop 0
	v_fma_f32 v1, -v0, v0, v1
	v_max_f32_e32 v1, 0, v1
	v_add_f32_e32 v1, 0x358637bd, v1
	v_mul_f32_e32 v33, 0x4b800000, v1
	v_cmp_gt_f32_e32 vcc, s89, v1
	v_sub_f32_e32 v18, v18, v0
	v_sub_f32_e32 v2, v2, v0
	v_cndmask_b32_e32 v1, v1, v33, vcc
	v_rsq_f32_e32 v1, v1
	v_bfe_u32 v33, v17, 16, 1
	v_add3_u32 v17, v17, v33, s90
	ds_write_b16_d16_hi v32, v17 offset:448
	v_mul_f32_e32 v17, 0x45800000, v1
	v_cndmask_b32_e32 v1, v1, v17, vcc
	v_mul_f32_e32 v18, v18, v1
	v_lshlrev_b32_e32 v17, 10, v217
	v_bfe_u32 v32, v18, 16, 1
	v_add3_u32 v18, v18, v32, s90
	v_add3_u32 v17, 0, v17, v16
	v_mul_f32_e32 v2, v2, v1
	ds_write_b16_d16_hi v17, v18
	v_bfe_u32 v18, v2, 16, 1
	v_add3_u32 v2, v2, v18, s90
	ds_write_b16_d16_hi v17, v2 offset:64
	v_sub_f32_e32 v2, v34, v0
	v_mul_f32_e32 v2, v2, v1
	v_bfe_u32 v18, v2, 16, 1
	v_add3_u32 v2, v2, v18, s90
	ds_write_b16_d16_hi v17, v2 offset:128
	v_sub_f32_e32 v2, v50, v0
	v_mul_f32_e32 v2, v2, v1
	v_bfe_u32 v18, v2, 16, 1
	v_add3_u32 v2, v2, v18, s90
	ds_write_b16_d16_hi v17, v2 offset:192
	v_sub_f32_e32 v2, v98, v0
	v_mul_f32_e32 v2, v2, v1
	v_bfe_u32 v18, v2, 16, 1
	v_add3_u32 v2, v2, v18, s90
	ds_write_b16_d16_hi v17, v2 offset:256
	v_sub_f32_e32 v2, v114, v0
	v_mul_f32_e32 v2, v2, v1
	v_bfe_u32 v18, v2, 16, 1
	v_add3_u32 v2, v2, v18, s90
	ds_write_b16_d16_hi v17, v2 offset:320
	v_sub_f32_e32 v2, v82, v0
	v_mul_f32_e32 v2, v2, v1
	v_bfe_u32 v18, v2, 16, 1
	v_add3_u32 v2, v2, v18, s90
	v_sub_f32_e32 v0, v66, v0
	ds_write_b16_d16_hi v17, v2 offset:384
	v_mul_f32_e32 v2, v0, v1
	v_pk_add_f32 v[0:1], v[154:155], v[170:171]
	s_nop 0
	v_pk_mul_f32 v[0:1], v[0:1], s[36:37] op_sel_hi:[1,0]
	s_nop 0
	v_fma_f32 v1, -v0, v0, v1
	v_max_f32_e32 v1, 0, v1
; #define LAS __attribute__((address_space(3)))
; __device__ __forceinline__ bf16_t f2bf(float f) { unsigned u = __builtin_bit_cast(unsigned, f); return (bf16_t)((u + 0x7fffu + ((u >> 16) & 1u)) >> 16); }
; __device__ __forceinline__ int crow(int r, int hi) { return (r & 3) + 8 * (r >> 2) + 4 * hi; }
; __device__ __forceinline__ int crow(int r, int hi) { return (r & 3) + 8 * (r >> 2) + 4 * hi; }
; template <int DK, int DV, bool MLSTM>
; __device__ __forceinline__ void out_unit2(LAS unsigned char* lds, LAS unsigned char* ldstab, const OutArgs a, const int wv) {
;     ...
;     for (int r = 0; r < 16; ++r) {
;         const int row = 32 * rb + crow(r, hi);
;         const float t1 = s1[r] + exch[((1 - dh) * 128 + row) * 2], t2 = s2[r] + exch[((1 - dh) * 128 + row) * 2 + 1];
;         float mean, inv;
;         if (MLSTM) { mean = 0.f; inv = rsqrtf(t2 * (1.f / DV) + EPS); }
;         else { mean = t1 * (1.f / DV); inv = rsqrtf(fmaxf(t2 * (1.f / DV) - mean * mean, 0.f) + EPS); }
; #pragma unroll
;         for (int nb = 0; nb < NB; ++nb) { const int col = dh * (DV / 2) + 32 * nb + r32;
;             *(LAS bf16_t*)(lds + row * TP + col * 2) = f2bf((o[nb][r] - mean) * inv); }
	v_add_f32_e32 v1, 0x358637bd, v1
	v_mul_f32_e32 v18, 0x4b800000, v1
	v_cmp_gt_f32_e32 vcc, s89, v1
	s_nop 1
	v_cndmask_b32_e32 v1, v1, v18, vcc
	v_rsq_f32_e32 v1, v1
	v_bfe_u32 v18, v2, 16, 1
	v_add3_u32 v2, v2, v18, s90
	ds_write_b16_d16_hi v17, v2 offset:448
	v_mul_f32_e32 v2, 0x45800000, v1
	v_cndmask_b32_e32 v1, v1, v2, vcc
	v_sub_f32_e32 v17, v19, v0
	v_mul_f32_e32 v17, v17, v1
	v_lshlrev_b32_e32 v2, 10, v216
	v_bfe_u32 v18, v17, 16, 1
	v_add3_u32 v17, v17, v18, s90
	v_add3_u32 v18, 0, v2, v16
	v_sub_f32_e32 v2, v3, v0
	v_mul_f32_e32 v2, v2, v1
	v_bfe_u32 v3, v2, 16, 1
	v_add3_u32 v2, v2, v3, s90
	ds_write_b16_d16_hi v18, v2 offset:64
	v_sub_f32_e32 v2, v35, v0
	v_mul_f32_e32 v2, v2, v1
	v_bfe_u32 v3, v2, 16, 1
	v_add3_u32 v2, v2, v3, s90
	ds_write_b16_d16_hi v18, v2 offset:128
	v_sub_f32_e32 v2, v51, v0
	v_mul_f32_e32 v2, v2, v1
	v_bfe_u32 v3, v2, 16, 1
	v_add3_u32 v2, v2, v3, s90
	ds_write_b16_d16_hi v18, v2 offset:192
	v_sub_f32_e32 v2, v99, v0
	v_mul_f32_e32 v2, v2, v1
	v_bfe_u32 v3, v2, 16, 1
	v_add3_u32 v2, v2, v3, s90
	ds_write_b16_d16_hi v18, v2 offset:256
	v_sub_f32_e32 v2, v115, v0
	v_mul_f32_e32 v2, v2, v1
	v_bfe_u32 v3, v2, 16, 1
	v_add3_u32 v2, v2, v3, s90
	ds_write_b16_d16_hi v18, v2 offset:320
	v_sub_f32_e32 v2, v83, v0
	v_sub_f32_e32 v0, v67, v0
	ds_write_b16_d16_hi v18, v17
	v_mul_f32_e32 v2, v2, v1
	v_mul_f32_e32 v17, v0, v1
	v_lshlrev_b32_e32 v0, 1, v215
	v_bfe_u32 v3, v2, 16, 1
	v_subrev_u32_e32 v0, s6, v0
	v_add3_u32 v2, v2, v3, s90
	v_lshl_add_u32 v0, v0, 2, s4
	ds_write_b16_d16_hi v18, v2 offset:384
	ds_read2_b64 v[0:3], v0 offset0:128 offset1:129
	v_lshlrev_b32_e32 v19, 1, v213
	v_subrev_u32_e32 v19, s6, v19
	v_lshl_add_u32 v19, v19, 2, s4
	ds_read2_b64 v[32:35], v19 offset0:128 offset1:129
	s_waitcnt lgkmcnt(1)
	v_pk_add_f32 v[0:1], v[148:149], v[0:1]
	s_nop 0
	v_pk_mul_f32 v[0:1], v[0:1], s[36:37] op_sel_hi:[1,0]
	s_nop 0
	v_fma_f32 v1, -v0, v0, v1
	v_max_f32_e32 v1, 0, v1
	v_add_f32_e32 v1, 0x358637bd, v1
	v_mul_f32_e32 v19, 0x4b800000, v1
	v_cmp_gt_f32_e32 vcc, s89, v1
	v_sub_f32_e32 v4, v4, v0
	s_nop 0
	v_cndmask_b32_e32 v1, v1, v19, vcc
	v_rsq_f32_e32 v1, v1
	v_bfe_u32 v19, v17, 16, 1
	v_add3_u32 v17, v17, v19, s90
	ds_write_b16_d16_hi v18, v17 offset:448
	v_mul_f32_e32 v17, 0x45800000, v1
	v_cndmask_b32_e32 v1, v1, v17, vcc
	v_sub_f32_e32 v18, v20, v0
	v_mul_f32_e32 v18, v18, v1
	v_lshlrev_b32_e32 v17, 10, v215
	v_bfe_u32 v19, v18, 16, 1
	v_add3_u32 v18, v18, v19, s90
	v_add3_u32 v17, 0, v17, v16
	v_mul_f32_e32 v4, v4, v1
	ds_write_b16_d16_hi v17, v18
	v_bfe_u32 v18, v4, 16, 1
	v_add3_u32 v4, v4, v18, s90
	ds_write_b16_d16_hi v17, v4 offset:64
	v_sub_f32_e32 v4, v36, v0
	v_mul_f32_e32 v4, v4, v1
	v_bfe_u32 v18, v4, 16, 1
	v_add3_u32 v4, v4, v18, s90
	ds_write_b16_d16_hi v17, v4 offset:128
	v_sub_f32_e32 v4, v52, v0
	v_mul_f32_e32 v4, v4, v1
	v_bfe_u32 v18, v4, 16, 1
	v_add3_u32 v4, v4, v18, s90
	ds_write_b16_d16_hi v17, v4 offset:192
	v_sub_f32_e32 v4, v100, v0
	v_mul_f32_e32 v4, v4, v1
	v_bfe_u32 v18, v4, 16, 1
	v_add3_u32 v4, v4, v18, s90
	ds_write_b16_d16_hi v17, v4 offset:256
	v_sub_f32_e32 v4, v116, v0
	v_mul_f32_e32 v4, v4, v1
	v_bfe_u32 v18, v4, 16, 1
	v_add3_u32 v4, v4, v18, s90
	ds_write_b16_d16_hi v17, v4 offset:320
	v_sub_f32_e32 v4, v84, v0
	v_mul_f32_e32 v4, v4, v1
	v_bfe_u32 v18, v4, 16, 1
	v_add3_u32 v4, v4, v18, s90
	v_sub_f32_e32 v0, v68, v0
	ds_write_b16_d16_hi v17, v4 offset:384
	v_mul_f32_e32 v4, v0, v1
	v_pk_add_f32 v[0:1], v[150:151], v[2:3]
	s_nop 0
	v_pk_mul_f32 v[0:1], v[0:1], s[36:37] op_sel_hi:[1,0]
	s_nop 0
	v_fma_f32 v1, -v0, v0, v1
	v_max_f32_e32 v1, 0, v1
	v_add_f32_e32 v1, 0x358637bd, v1
	v_mul_f32_e32 v2, 0x4b800000, v1
	v_cmp_gt_f32_e32 vcc, s89, v1
	v_sub_f32_e32 v3, v21, v0
	s_nop 0
	v_cndmask_b32_e32 v1, v1, v2, vcc
	v_rsq_f32_e32 v1, v1
	v_bfe_u32 v2, v4, 16, 1
	v_add3_u32 v2, v4, v2, s90
	ds_write_b16_d16_hi v17, v2 offset:448
	v_mul_f32_e32 v2, 0x45800000, v1
	v_cndmask_b32_e32 v1, v1, v2, vcc
	v_mul_f32_e32 v3, v3, v1
	v_lshlrev_b32_e32 v2, 10, v214
	v_bfe_u32 v4, v3, 16, 1
	v_add3_u32 v3, v3, v4, s90
	v_add3_u32 v2, 0, v2, v16
	ds_write_b16_d16_hi v2, v3
	v_sub_f32_e32 v3, v5, v0
	v_mul_f32_e32 v3, v3, v1
	v_bfe_u32 v4, v3, 16, 1
	v_add3_u32 v3, v3, v4, s90
	ds_write_b16_d16_hi v2, v3 offset:64
	v_sub_f32_e32 v3, v37, v0
	v_mul_f32_e32 v3, v3, v1
	v_bfe_u32 v4, v3, 16, 1
	v_add3_u32 v3, v3, v4, s90
	ds_write_b16_d16_hi v2, v3 offset:128
	v_sub_f32_e32 v3, v53, v0
	v_mul_f32_e32 v3, v3, v1
	v_bfe_u32 v4, v3, 16, 1
	v_add3_u32 v3, v3, v4, s90
	ds_write_b16_d16_hi v2, v3 offset:192
	v_sub_f32_e32 v3, v101, v0
	v_mul_f32_e32 v3, v3, v1
	v_bfe_u32 v4, v3, 16, 1
	v_add3_u32 v3, v3, v4, s90
	ds_write_b16_d16_hi v2, v3 offset:256
	v_sub_f32_e32 v3, v117, v0
	v_mul_f32_e32 v3, v3, v1
	v_bfe_u32 v4, v3, 16, 1
	v_add3_u32 v3, v3, v4, s90
	ds_write_b16_d16_hi v2, v3 offset:320
	v_sub_f32_e32 v3, v85, v0
	v_mul_f32_e32 v3, v3, v1
	v_bfe_u32 v4, v3, 16, 1
	v_add3_u32 v3, v3, v4, s90
	v_sub_f32_e32 v0, v69, v0
	ds_write_b16_d16_hi v2, v3 offset:384
	v_mul_f32_e32 v3, v0, v1
	s_waitcnt lgkmcnt(14)
; #define LAS __attribute__((address_space(3)))
; __device__ __forceinline__ bf16_t f2bf(float f) { unsigned u = __builtin_bit_cast(unsigned, f); return (bf16_t)((u + 0x7fffu + ((u >> 16) & 1u)) >> 16); }
; __device__ __forceinline__ int crow(int r, int hi) { return (r & 3) + 8 * (r >> 2) + 4 * hi; }
; __device__ __forceinline__ int crow(int r, int hi) { return (r & 3) + 8 * (r >> 2) + 4 * hi; }
; template <int DK, int DV, bool MLSTM>
; __device__ __forceinline__ void out_unit2(LAS unsigned char* lds, LAS unsigned char* ldstab, const OutArgs a, const int wv) {
;     ...
;     for (int r = 0; r < 16; ++r) {
;         const int row = 32 * rb + crow(r, hi);
;         const float t1 = s1[r] + exch[((1 - dh) * 128 + row) * 2], t2 = s2[r] + exch[((1 - dh) * 128 + row) * 2 + 1];
;         float mean, inv;
;         if (MLSTM) { mean = 0.f; inv = rsqrtf(t2 * (1.f / DV) + EPS); }
;         else { mean = t1 * (1.f / DV); inv = rsqrtf(fmaxf(t2 * (1.f / DV) - mean * mean, 0.f) + EPS); }
; #pragma unroll
;         for (int nb = 0; nb < NB; ++nb) { const int col = dh * (DV / 2) + 32 * nb + r32;
;             *(LAS bf16_t*)(lds + row * TP + col * 2) = f2bf((o[nb][r] - mean) * inv); }
	v_pk_add_f32 v[0:1], v[144:145], v[32:33]
	s_nop 0
	v_pk_mul_f32 v[0:1], v[0:1], s[36:37] op_sel_hi:[1,0]
	s_nop 0
	v_fma_f32 v1, -v0, v0, v1
	v_max_f32_e32 v1, 0, v1
	v_add_f32_e32 v1, 0x358637bd, v1
	v_mul_f32_e32 v4, 0x4b800000, v1
	v_cmp_gt_f32_e32 vcc, s89, v1
	s_nop 1
	v_cndmask_b32_e32 v1, v1, v4, vcc
	v_rsq_f32_e32 v1, v1
	v_bfe_u32 v4, v3, 16, 1
	v_add3_u32 v3, v3, v4, s90
	ds_write_b16_d16_hi v2, v3 offset:448
	v_mul_f32_e32 v2, 0x45800000, v1
	v_cndmask_b32_e32 v1, v1, v2, vcc
	v_sub_f32_e32 v3, v22, v0
	v_mul_f32_e32 v3, v3, v1
	v_lshlrev_b32_e32 v2, 10, v213
	v_bfe_u32 v4, v3, 16, 1
	v_add3_u32 v3, v3, v4, s90
	v_add3_u32 v2, 0, v2, v16
	ds_write_b16_d16_hi v2, v3
	v_sub_f32_e32 v3, v6, v0
	v_mul_f32_e32 v3, v3, v1
	v_bfe_u32 v4, v3, 16, 1
	v_add3_u32 v3, v3, v4, s90
	ds_write_b16_d16_hi v2, v3 offset:64
	v_sub_f32_e32 v3, v38, v0
	v_mul_f32_e32 v3, v3, v1
	v_bfe_u32 v4, v3, 16, 1
	v_add3_u32 v3, v3, v4, s90
	ds_write_b16_d16_hi v2, v3 offset:128
	v_sub_f32_e32 v3, v54, v0
	v_mul_f32_e32 v3, v3, v1
	v_bfe_u32 v4, v3, 16, 1
	v_add3_u32 v3, v3, v4, s90
	ds_write_b16_d16_hi v2, v3 offset:192
	v_sub_f32_e32 v3, v102, v0
	v_mul_f32_e32 v3, v3, v1
	v_bfe_u32 v4, v3, 16, 1
	v_add3_u32 v3, v3, v4, s90
	ds_write_b16_d16_hi v2, v3 offset:256
	v_sub_f32_e32 v3, v118, v0
	v_mul_f32_e32 v3, v3, v1
	v_bfe_u32 v4, v3, 16, 1
	v_add3_u32 v3, v3, v4, s90
	ds_write_b16_d16_hi v2, v3 offset:320
	v_sub_f32_e32 v3, v86, v0
	v_mul_f32_e32 v3, v3, v1
	v_bfe_u32 v4, v3, 16, 1
	v_add3_u32 v3, v3, v4, s90
	v_sub_f32_e32 v0, v70, v0
	ds_write_b16_d16_hi v2, v3 offset:384
	v_mul_f32_e32 v3, v0, v1
	v_pk_add_f32 v[0:1], v[146:147], v[34:35]
	s_nop 0
	v_pk_mul_f32 v[0:1], v[0:1], s[36:37] op_sel_hi:[1,0]
	s_nop 0
	v_fma_f32 v1, -v0, v0, v1
	v_max_f32_e32 v1, 0, v1
	v_add_f32_e32 v1, 0x358637bd, v1
	v_mul_f32_e32 v4, 0x4b800000, v1
	v_cmp_gt_f32_e32 vcc, s89, v1
	s_nop 1
	v_cndmask_b32_e32 v1, v1, v4, vcc
	v_rsq_f32_e32 v1, v1
	v_bfe_u32 v4, v3, 16, 1
	v_add3_u32 v3, v3, v4, s90
	ds_write_b16_d16_hi v2, v3 offset:448
	v_mul_f32_e32 v2, 0x45800000, v1
	v_cndmask_b32_e32 v1, v1, v2, vcc
	v_sub_f32_e32 v3, v23, v0
	v_lshlrev_b32_e32 v2, 10, v212
	v_mul_f32_e32 v3, v3, v1
	v_bfe_u32 v4, v3, 16, 1
	v_add3_u32 v17, 0, v2, v16
	v_sub_f32_e32 v2, v7, v0
	v_add3_u32 v3, v3, v4, s90
	v_mul_f32_e32 v2, v2, v1
	ds_write_b16_d16_hi v17, v3
	v_bfe_u32 v3, v2, 16, 1
	v_add3_u32 v2, v2, v3, s90
	ds_write_b16_d16_hi v17, v2 offset:64
	v_sub_f32_e32 v2, v39, v0
	v_mul_f32_e32 v2, v2, v1
	v_bfe_u32 v3, v2, 16, 1
	v_add3_u32 v2, v2, v3, s90
	ds_write_b16_d16_hi v17, v2 offset:128
	v_sub_f32_e32 v2, v55, v0
	v_mul_f32_e32 v2, v2, v1
	v_bfe_u32 v3, v2, 16, 1
	v_add3_u32 v2, v2, v3, s90
	ds_write_b16_d16_hi v17, v2 offset:192
	v_sub_f32_e32 v2, v103, v0
	v_mul_f32_e32 v2, v2, v1
	v_bfe_u32 v3, v2, 16, 1
	v_add3_u32 v2, v2, v3, s90
	ds_write_b16_d16_hi v17, v2 offset:256
	v_sub_f32_e32 v2, v119, v0
	v_mul_f32_e32 v2, v2, v1
	v_bfe_u32 v3, v2, 16, 1
	v_add3_u32 v2, v2, v3, s90
	ds_write_b16_d16_hi v17, v2 offset:320
	v_sub_f32_e32 v2, v87, v0
	v_sub_f32_e32 v0, v71, v0
	v_mul_f32_e32 v2, v2, v1
	v_mul_f32_e32 v18, v0, v1
	v_lshlrev_b32_e32 v0, 1, v211
	v_bfe_u32 v3, v2, 16, 1
	v_subrev_u32_e32 v0, s6, v0
	v_add3_u32 v2, v2, v3, s90
	v_lshl_add_u32 v0, v0, 2, s4
	ds_write_b16_d16_hi v17, v2 offset:384
	ds_read2_b64 v[0:3], v0 offset0:128 offset1:129
	v_lshlrev_b32_e32 v4, 1, v209
	v_subrev_u32_e32 v4, s6, v4
	v_lshl_add_u32 v4, v4, 2, s4
	ds_read2_b64 v[4:7], v4 offset0:128 offset1:129
	s_waitcnt lgkmcnt(1)
	v_pk_add_f32 v[0:1], v[140:141], v[0:1]
	s_nop 0
	v_pk_mul_f32 v[0:1], v[0:1], s[36:37] op_sel_hi:[1,0]
	s_nop 0
	v_fma_f32 v1, -v0, v0, v1
	v_max_f32_e32 v1, 0, v1
	v_add_f32_e32 v1, 0x358637bd, v1
	v_mul_f32_e32 v19, 0x4b800000, v1
	v_cmp_gt_f32_e32 vcc, s89, v1
	v_sub_f32_e32 v8, v8, v0
	s_nop 0
	v_cndmask_b32_e32 v1, v1, v19, vcc
	v_rsq_f32_e32 v1, v1
	v_bfe_u32 v19, v18, 16, 1
	v_add3_u32 v18, v18, v19, s90
	ds_write_b16_d16_hi v17, v18 offset:448
	v_mul_f32_e32 v17, 0x45800000, v1
	v_cndmask_b32_e32 v1, v1, v17, vcc
	v_sub_f32_e32 v18, v24, v0
	v_mul_f32_e32 v18, v18, v1
	v_lshlrev_b32_e32 v17, 10, v211
	v_bfe_u32 v19, v18, 16, 1
	v_add3_u32 v18, v18, v19, s90
	v_add3_u32 v17, 0, v17, v16
	v_mul_f32_e32 v8, v8, v1
	ds_write_b16_d16_hi v17, v18
	v_bfe_u32 v18, v8, 16, 1
	v_add3_u32 v8, v8, v18, s90
	ds_write_b16_d16_hi v17, v8 offset:64
	v_sub_f32_e32 v8, v40, v0
	v_mul_f32_e32 v8, v8, v1
	v_bfe_u32 v18, v8, 16, 1
	v_add3_u32 v8, v8, v18, s90
	ds_write_b16_d16_hi v17, v8 offset:128
	v_sub_f32_e32 v8, v56, v0
	v_mul_f32_e32 v8, v8, v1
	v_bfe_u32 v18, v8, 16, 1
	v_add3_u32 v8, v8, v18, s90
	ds_write_b16_d16_hi v17, v8 offset:192
	v_sub_f32_e32 v8, v104, v0
	v_mul_f32_e32 v8, v8, v1
	v_bfe_u32 v18, v8, 16, 1
	v_add3_u32 v8, v8, v18, s90
	ds_write_b16_d16_hi v17, v8 offset:256
	v_sub_f32_e32 v8, v120, v0
	v_mul_f32_e32 v8, v8, v1
	v_bfe_u32 v18, v8, 16, 1
	v_add3_u32 v8, v8, v18, s90
	ds_write_b16_d16_hi v17, v8 offset:320
	v_sub_f32_e32 v8, v88, v0
	v_mul_f32_e32 v8, v8, v1
	v_bfe_u32 v18, v8, 16, 1
	v_add3_u32 v8, v8, v18, s90
	v_sub_f32_e32 v0, v72, v0
	ds_write_b16_d16_hi v17, v8 offset:384
	v_mul_f32_e32 v8, v0, v1
	v_pk_add_f32 v[0:1], v[142:143], v[2:3]
	s_nop 0
	v_pk_mul_f32 v[0:1], v[0:1], s[36:37] op_sel_hi:[1,0]
	s_nop 0
	v_fma_f32 v1, -v0, v0, v1
	v_max_f32_e32 v1, 0, v1
	v_add_f32_e32 v1, 0x358637bd, v1
	v_mul_f32_e32 v2, 0x4b800000, v1
	v_cmp_gt_f32_e32 vcc, s89, v1
	v_sub_f32_e32 v3, v25, v0
	s_nop 0
	v_cndmask_b32_e32 v1, v1, v2, vcc
	v_rsq_f32_e32 v1, v1
	v_bfe_u32 v2, v8, 16, 1
	v_add3_u32 v2, v8, v2, s90
	ds_write_b16_d16_hi v17, v2 offset:448
	v_mul_f32_e32 v2, 0x45800000, v1
	v_cndmask_b32_e32 v1, v1, v2, vcc
	v_mul_f32_e32 v3, v3, v1
	v_lshlrev_b32_e32 v2, 10, v210
	v_bfe_u32 v8, v3, 16, 1
	v_add3_u32 v3, v3, v8, s90
	v_add3_u32 v2, 0, v2, v16
	ds_write_b16_d16_hi v2, v3
	v_sub_f32_e32 v3, v9, v0
	v_mul_f32_e32 v3, v3, v1
	v_bfe_u32 v8, v3, 16, 1
	v_add3_u32 v3, v3, v8, s90
	ds_write_b16_d16_hi v2, v3 offset:64
	v_sub_f32_e32 v3, v41, v0
	v_mul_f32_e32 v3, v3, v1
	v_bfe_u32 v8, v3, 16, 1
	v_add3_u32 v3, v3, v8, s90
	ds_write_b16_d16_hi v2, v3 offset:128
	v_sub_f32_e32 v3, v57, v0
	v_mul_f32_e32 v3, v3, v1
	v_bfe_u32 v8, v3, 16, 1
	v_add3_u32 v3, v3, v8, s90
	ds_write_b16_d16_hi v2, v3 offset:192
	v_sub_f32_e32 v3, v105, v0
	v_mul_f32_e32 v3, v3, v1
	v_bfe_u32 v8, v3, 16, 1
	v_add3_u32 v3, v3, v8, s90
	ds_write_b16_d16_hi v2, v3 offset:256
	v_sub_f32_e32 v3, v121, v0
	v_mul_f32_e32 v3, v3, v1
	v_bfe_u32 v8, v3, 16, 1
	v_add3_u32 v3, v3, v8, s90
	ds_write_b16_d16_hi v2, v3 offset:320
	v_sub_f32_e32 v3, v89, v0
	v_mul_f32_e32 v3, v3, v1
	v_bfe_u32 v8, v3, 16, 1
	v_add3_u32 v3, v3, v8, s90
	v_sub_f32_e32 v0, v73, v0
	ds_write_b16_d16_hi v2, v3 offset:384
	v_mul_f32_e32 v3, v0, v1
	s_waitcnt lgkmcnt(14)
; #define LAS __attribute__((address_space(3)))
; __device__ __forceinline__ bf16_t f2bf(float f) { unsigned u = __builtin_bit_cast(unsigned, f); return (bf16_t)((u + 0x7fffu + ((u >> 16) & 1u)) >> 16); }
; __device__ __forceinline__ int crow(int r, int hi) { return (r & 3) + 8 * (r >> 2) + 4 * hi; }
; __device__ __forceinline__ int crow(int r, int hi) { return (r & 3) + 8 * (r >> 2) + 4 * hi; }
; template <int DK, int DV, bool MLSTM>
; __device__ __forceinline__ void out_unit2(LAS unsigned char* lds, LAS unsigned char* ldstab, const OutArgs a, const int wv) {
;     ...
;     for (int r = 0; r < 16; ++r) {
;         const int row = 32 * rb + crow(r, hi);
;         const float t1 = s1[r] + exch[((1 - dh) * 128 + row) * 2], t2 = s2[r] + exch[((1 - dh) * 128 + row) * 2 + 1];
;         float mean, inv;
;         if (MLSTM) { mean = 0.f; inv = rsqrtf(t2 * (1.f / DV) + EPS); }
;         else { mean = t1 * (1.f / DV); inv = rsqrtf(fmaxf(t2 * (1.f / DV) - mean * mean, 0.f) + EPS); }
; #pragma unroll
;         for (int nb = 0; nb < NB; ++nb) { const int col = dh * (DV / 2) + 32 * nb + r32;
;             *(LAS bf16_t*)(lds + row * TP + col * 2) = f2bf((o[nb][r] - mean) * inv); }
	v_pk_add_f32 v[0:1], v[136:137], v[4:5]
	s_nop 0
	v_pk_mul_f32 v[0:1], v[0:1], s[36:37] op_sel_hi:[1,0]
	s_nop 0
	v_fma_f32 v1, -v0, v0, v1
	v_max_f32_e32 v1, 0, v1
	v_add_f32_e32 v1, 0x358637bd, v1
	v_mul_f32_e32 v4, 0x4b800000, v1
	v_cmp_gt_f32_e32 vcc, s89, v1
	s_nop 1
	v_cndmask_b32_e32 v1, v1, v4, vcc
	v_rsq_f32_e32 v1, v1
	v_bfe_u32 v4, v3, 16, 1
	v_add3_u32 v3, v3, v4, s90
	ds_write_b16_d16_hi v2, v3 offset:448
	v_mul_f32_e32 v2, 0x45800000, v1
	v_cndmask_b32_e32 v1, v1, v2, vcc
	v_sub_f32_e32 v3, v26, v0
	v_mul_f32_e32 v3, v3, v1
	v_lshlrev_b32_e32 v2, 10, v209
	v_bfe_u32 v4, v3, 16, 1
	v_add3_u32 v3, v3, v4, s90
	v_add3_u32 v2, 0, v2, v16
	ds_write_b16_d16_hi v2, v3
	v_sub_f32_e32 v3, v10, v0
	v_mul_f32_e32 v3, v3, v1
	v_bfe_u32 v4, v3, 16, 1
	v_add3_u32 v3, v3, v4, s90
	ds_write_b16_d16_hi v2, v3 offset:64
	v_sub_f32_e32 v3, v42, v0
	v_mul_f32_e32 v3, v3, v1
	v_bfe_u32 v4, v3, 16, 1
	v_add3_u32 v3, v3, v4, s90
	ds_write_b16_d16_hi v2, v3 offset:128
	v_sub_f32_e32 v3, v58, v0
	v_mul_f32_e32 v3, v3, v1
	v_bfe_u32 v4, v3, 16, 1
	v_add3_u32 v3, v3, v4, s90
	ds_write_b16_d16_hi v2, v3 offset:192
	v_sub_f32_e32 v3, v106, v0
	v_mul_f32_e32 v3, v3, v1
	v_bfe_u32 v4, v3, 16, 1
	v_add3_u32 v3, v3, v4, s90
	ds_write_b16_d16_hi v2, v3 offset:256
	v_sub_f32_e32 v3, v122, v0
	v_mul_f32_e32 v3, v3, v1
	v_bfe_u32 v4, v3, 16, 1
	v_add3_u32 v3, v3, v4, s90
	ds_write_b16_d16_hi v2, v3 offset:320
	v_sub_f32_e32 v3, v90, v0
	v_mul_f32_e32 v3, v3, v1
	v_bfe_u32 v4, v3, 16, 1
	v_add3_u32 v3, v3, v4, s90
	v_sub_f32_e32 v0, v74, v0
	ds_write_b16_d16_hi v2, v3 offset:384
	v_mul_f32_e32 v3, v0, v1
	v_pk_add_f32 v[0:1], v[138:139], v[6:7]
	s_nop 0
	v_pk_mul_f32 v[0:1], v[0:1], s[36:37] op_sel_hi:[1,0]
	s_nop 0
	v_fma_f32 v1, -v0, v0, v1
	v_max_f32_e32 v1, 0, v1
	v_add_f32_e32 v1, 0x358637bd, v1
	v_mul_f32_e32 v4, 0x4b800000, v1
	v_cmp_gt_f32_e32 vcc, s89, v1
	s_nop 1
	v_cndmask_b32_e32 v1, v1, v4, vcc
	v_rsq_f32_e32 v1, v1
	v_bfe_u32 v4, v3, 16, 1
	v_add3_u32 v3, v3, v4, s90
	ds_write_b16_d16_hi v2, v3 offset:448
	v_mul_f32_e32 v2, 0x45800000, v1
	v_cndmask_b32_e32 v1, v1, v2, vcc
	v_sub_f32_e32 v3, v27, v0
	v_lshlrev_b32_e32 v2, 10, v208
	v_mul_f32_e32 v3, v3, v1
	v_bfe_u32 v4, v3, 16, 1
	v_add3_u32 v8, 0, v2, v16
	v_sub_f32_e32 v2, v11, v0
	v_add3_u32 v3, v3, v4, s90
	v_mul_f32_e32 v2, v2, v1
	ds_write_b16_d16_hi v8, v3
	v_bfe_u32 v3, v2, 16, 1
	v_add3_u32 v2, v2, v3, s90
	ds_write_b16_d16_hi v8, v2 offset:64
	v_sub_f32_e32 v2, v43, v0
	v_mul_f32_e32 v2, v2, v1
	v_bfe_u32 v3, v2, 16, 1
	v_add3_u32 v2, v2, v3, s90
	ds_write_b16_d16_hi v8, v2 offset:128
	v_sub_f32_e32 v2, v59, v0
	v_mul_f32_e32 v2, v2, v1
	v_bfe_u32 v3, v2, 16, 1
	v_add3_u32 v2, v2, v3, s90
	ds_write_b16_d16_hi v8, v2 offset:192
	v_sub_f32_e32 v2, v107, v0
	v_mul_f32_e32 v2, v2, v1
	v_bfe_u32 v3, v2, 16, 1
	v_add3_u32 v2, v2, v3, s90
	ds_write_b16_d16_hi v8, v2 offset:256
	v_sub_f32_e32 v2, v123, v0
	v_mul_f32_e32 v2, v2, v1
	v_bfe_u32 v3, v2, 16, 1
	v_add3_u32 v2, v2, v3, s90
	ds_write_b16_d16_hi v8, v2 offset:320
	v_sub_f32_e32 v2, v91, v0
	v_sub_f32_e32 v0, v75, v0
	v_mul_f32_e32 v2, v2, v1
	v_mul_f32_e32 v9, v0, v1
	v_lshlrev_b32_e32 v0, 1, v207
	v_bfe_u32 v3, v2, 16, 1
	v_subrev_u32_e32 v0, s6, v0
	v_add3_u32 v2, v2, v3, s90
	v_lshl_add_u32 v0, v0, 2, s4
	ds_write_b16_d16_hi v8, v2 offset:384
	ds_read2_b64 v[0:3], v0 offset0:128 offset1:129
	v_lshlrev_b32_e32 v4, 1, v162
	v_subrev_u32_e32 v4, s6, v4
	v_lshl_add_u32 v4, v4, 2, s4
	ds_read2_b64 v[4:7], v4 offset0:128 offset1:129
	s_waitcnt lgkmcnt(1)
	v_pk_add_f32 v[0:1], v[132:133], v[0:1]
	s_nop 0
	v_pk_mul_f32 v[0:1], v[0:1], s[36:37] op_sel_hi:[1,0]
	s_nop 0
	v_fma_f32 v1, -v0, v0, v1
	v_max_f32_e32 v1, 0, v1
	v_add_f32_e32 v1, 0x358637bd, v1
	v_mul_f32_e32 v10, 0x4b800000, v1
	v_cmp_gt_f32_e32 vcc, s89, v1
	s_nop 1
	v_cndmask_b32_e32 v1, v1, v10, vcc
	v_rsq_f32_e32 v1, v1
	v_bfe_u32 v10, v9, 16, 1
	v_add3_u32 v9, v9, v10, s90
	ds_write_b16_d16_hi v8, v9 offset:448
	v_mul_f32_e32 v8, 0x45800000, v1
	v_cndmask_b32_e32 v1, v1, v8, vcc
	v_sub_f32_e32 v9, v28, v0
	v_mul_f32_e32 v9, v9, v1
	v_lshlrev_b32_e32 v8, 10, v207
	v_bfe_u32 v10, v9, 16, 1
	v_add3_u32 v9, v9, v10, s90
	v_add3_u32 v8, 0, v8, v16
	ds_write_b16_d16_hi v8, v9
	v_sub_f32_e32 v9, v12, v0
	v_mul_f32_e32 v9, v9, v1
	v_bfe_u32 v10, v9, 16, 1
	v_add3_u32 v9, v9, v10, s90
	ds_write_b16_d16_hi v8, v9 offset:64
	v_sub_f32_e32 v9, v44, v0
	v_mul_f32_e32 v9, v9, v1
	v_bfe_u32 v10, v9, 16, 1
	v_add3_u32 v9, v9, v10, s90
	ds_write_b16_d16_hi v8, v9 offset:128
	v_sub_f32_e32 v9, v60, v0
	v_mul_f32_e32 v9, v9, v1
	v_bfe_u32 v10, v9, 16, 1
	v_add3_u32 v9, v9, v10, s90
	ds_write_b16_d16_hi v8, v9 offset:192
	v_sub_f32_e32 v9, v108, v0
	v_mul_f32_e32 v9, v9, v1
	v_bfe_u32 v10, v9, 16, 1
	v_add3_u32 v9, v9, v10, s90
	ds_write_b16_d16_hi v8, v9 offset:256
	v_sub_f32_e32 v9, v124, v0
	v_mul_f32_e32 v9, v9, v1
	v_bfe_u32 v10, v9, 16, 1
	v_add3_u32 v9, v9, v10, s90
	ds_write_b16_d16_hi v8, v9 offset:320
	v_sub_f32_e32 v9, v92, v0
	v_mul_f32_e32 v9, v9, v1
	v_bfe_u32 v10, v9, 16, 1
	v_add3_u32 v9, v9, v10, s90
	v_sub_f32_e32 v0, v76, v0
	ds_write_b16_d16_hi v8, v9 offset:384
	v_mul_f32_e32 v9, v0, v1
	v_pk_add_f32 v[0:1], v[134:135], v[2:3]
	s_nop 0
	v_pk_mul_f32 v[0:1], v[0:1], s[36:37] op_sel_hi:[1,0]
	s_nop 0
	v_fma_f32 v1, -v0, v0, v1
	v_max_f32_e32 v1, 0, v1
	v_add_f32_e32 v1, 0x358637bd, v1
	v_mul_f32_e32 v2, 0x4b800000, v1
	v_cmp_gt_f32_e32 vcc, s89, v1
	v_sub_f32_e32 v3, v29, v0
	s_nop 0
	v_cndmask_b32_e32 v1, v1, v2, vcc
	v_rsq_f32_e32 v1, v1
	v_bfe_u32 v2, v9, 16, 1
	v_add3_u32 v2, v9, v2, s90
	ds_write_b16_d16_hi v8, v2 offset:448
	v_mul_f32_e32 v2, 0x45800000, v1
	v_cndmask_b32_e32 v1, v1, v2, vcc
	v_mul_f32_e32 v3, v3, v1
	v_lshlrev_b32_e32 v2, 10, v206
	v_bfe_u32 v8, v3, 16, 1
	v_add3_u32 v3, v3, v8, s90
	v_add3_u32 v2, 0, v2, v16
	ds_write_b16_d16_hi v2, v3
	v_sub_f32_e32 v3, v13, v0
	v_mul_f32_e32 v3, v3, v1
	v_bfe_u32 v8, v3, 16, 1
	v_add3_u32 v3, v3, v8, s90
	ds_write_b16_d16_hi v2, v3 offset:64
	v_sub_f32_e32 v3, v45, v0
	v_mul_f32_e32 v3, v3, v1
	v_bfe_u32 v8, v3, 16, 1
	v_add3_u32 v3, v3, v8, s90
	ds_write_b16_d16_hi v2, v3 offset:128
	v_sub_f32_e32 v3, v61, v0
	v_mul_f32_e32 v3, v3, v1
	v_bfe_u32 v8, v3, 16, 1
	v_add3_u32 v3, v3, v8, s90
	ds_write_b16_d16_hi v2, v3 offset:192
	v_sub_f32_e32 v3, v109, v0
	v_mul_f32_e32 v3, v3, v1
	v_bfe_u32 v8, v3, 16, 1
	v_add3_u32 v3, v3, v8, s90
	ds_write_b16_d16_hi v2, v3 offset:256
	v_sub_f32_e32 v3, v125, v0
	v_mul_f32_e32 v3, v3, v1
	v_bfe_u32 v8, v3, 16, 1
	v_add3_u32 v3, v3, v8, s90
	ds_write_b16_d16_hi v2, v3 offset:320
	v_sub_f32_e32 v3, v93, v0
	v_mul_f32_e32 v3, v3, v1
	v_bfe_u32 v8, v3, 16, 1
	v_add3_u32 v3, v3, v8, s90
	v_sub_f32_e32 v0, v77, v0
	ds_write_b16_d16_hi v2, v3 offset:384
	v_mul_f32_e32 v3, v0, v1
	s_waitcnt lgkmcnt(14)
; #define LAS __attribute__((address_space(3)))
; template <int DK, int DV, bool MLSTM>
; __device__ __forceinline__ void out_unit2(LAS unsigned char* lds, LAS unsigned char* ldstab, const OutArgs a, const int wv) {
;     ...
;     for (int r = 0; r < 16; ++r) {
;         const int row = 32 * rb + crow(r, hi);
;         const float t1 = s1[r] + exch[((1 - dh) * 128 + row) * 2], t2 = s2[r] + exch[((1 - dh) * 128 + row) * 2 + 1];
;         float mean, inv;
;         if (MLSTM) { mean = 0.f; inv = rsqrtf(t2 * (1.f / DV) + EPS); }
;         else { mean = t1 * (1.f / DV); inv = rsqrtf(fmaxf(t2 * (1.f / DV) - mean * mean, 0.f) + EPS); }
; #pragma unroll
;         for (int nb = 0; nb < NB; ++nb) { const int col = dh * (DV / 2) + 32 * nb + r32;
;             *(LAS bf16_t*)(lds + row * TP + col * 2) = f2bf((o[nb][r] - mean) * inv); }
;     }
;     __syncthreads();
;     constexpr int CPR = DV / 8;
; #pragma unroll 1
;     for (int id = tid; id < 128 * CPR; id += 512) { const int row = id / CPR, ch = id % CPR;
;         const u32x4 y = *(const LAS u32x4*)(lds + row * TP + ch * 16);
;         const f32x4 g0 = *(const f32x4*)(a.gain + 8 * ch), g1 = *(const f32x4*)(a.gain + 8 * ch + 4);
;         float yv[8] = {bf_lo(y.x), bf_hi(y.x), bf_lo(y.y), bf_hi(y.y), bf_lo(y.z), bf_hi(y.z), bf_lo(y.w), bf_hi(y.w)};
;         float gv[8];
;         if (MLSTM) { const u32x4 g = *(const u32x4*)(a.G + (size_t)row * a.ldg + 8 * ch);
;             gv[0] = bf_lo(g.x); gv[1] = bf_hi(g.x); gv[2] = bf_lo(g.y); gv[3] = bf_hi(g.y); gv[4] = bf_lo(g.z); gv[5] = bf_hi(g.z); gv[6] = bf_lo(g.w); gv[7] = bf_hi(g.w); }
;         else { const u32x2 g = *(const u32x2*)(a.G8 + (size_t)row * a.ldg8 + 8 * ch);
;             const f32x2 e0 = __builtin_amdgcn_cvt_pk_f32_fp8((int)g.x, false), e1 = __builtin_amdgcn_cvt_pk_f32_fp8((int)g.x, true), e2 = __builtin_amdgcn_cvt_pk_f32_fp8((int)g.y, false), e3 = __builtin_amdgcn_cvt_pk_f32_fp8((int)g.y, true);
;             gv[0] = e0[0] * a.g8inv; gv[1] = e0[1] * a.g8inv; gv[2] = e1[0] * a.g8inv; gv[3] = e1[1] * a.g8inv; gv[4] = e2[0] * a.g8inv; gv[5] = e2[1] * a.g8inv; gv[6] = e3[0] * a.g8inv; gv[7] = e3[1] * a.g8inv; }
;         float gn[8] = {g0[0], g0[1], g0[2], g0[3], g1[0], g1[1], g1[2], g1[3]};
;         float ov[8];
; #pragma unroll
;         for (int i = 0; i < 8; ++i) ov[i] = yv[i] * gn[i] * (MLSTM ? sigmoidf_(gv[i]) : siluf_(gv[i]));
	v_pk_add_f32 v[0:1], v[128:129], v[4:5]
	s_nop 0
	v_pk_mul_f32 v[0:1], v[0:1], s[36:37] op_sel_hi:[1,0]
	s_nop 0
	v_fma_f32 v1, -v0, v0, v1
	v_max_f32_e32 v1, 0, v1
	v_add_f32_e32 v1, 0x358637bd, v1
	v_mul_f32_e32 v4, 0x4b800000, v1
	v_cmp_gt_f32_e32 vcc, s89, v1
	s_nop 1
	v_cndmask_b32_e32 v1, v1, v4, vcc
	v_rsq_f32_e32 v1, v1
	v_bfe_u32 v4, v3, 16, 1
	v_add3_u32 v3, v3, v4, s90
	ds_write_b16_d16_hi v2, v3 offset:448
	v_mul_f32_e32 v2, 0x45800000, v1
	v_cndmask_b32_e32 v1, v1, v2, vcc
	v_sub_f32_e32 v3, v30, v0
	v_mul_f32_e32 v3, v3, v1
	v_lshlrev_b32_e32 v2, 10, v162
	v_bfe_u32 v4, v3, 16, 1
	v_add3_u32 v3, v3, v4, s90
	v_add3_u32 v2, 0, v2, v16
	ds_write_b16_d16_hi v2, v3
	v_sub_f32_e32 v3, v14, v0
	v_mul_f32_e32 v3, v3, v1
	v_bfe_u32 v4, v3, 16, 1
	v_add3_u32 v3, v3, v4, s90
	ds_write_b16_d16_hi v2, v3 offset:64
	v_sub_f32_e32 v3, v46, v0
	v_mul_f32_e32 v3, v3, v1
	v_bfe_u32 v4, v3, 16, 1
	v_add3_u32 v3, v3, v4, s90
	ds_write_b16_d16_hi v2, v3 offset:128
	v_sub_f32_e32 v3, v62, v0
	v_mul_f32_e32 v3, v3, v1
	v_bfe_u32 v4, v3, 16, 1
	v_add3_u32 v3, v3, v4, s90
	ds_write_b16_d16_hi v2, v3 offset:192
	v_sub_f32_e32 v3, v110, v0
	v_mul_f32_e32 v3, v3, v1
	v_bfe_u32 v4, v3, 16, 1
	v_add3_u32 v3, v3, v4, s90
	ds_write_b16_d16_hi v2, v3 offset:256
	v_sub_f32_e32 v3, v126, v0
	v_mul_f32_e32 v3, v3, v1
	v_bfe_u32 v4, v3, 16, 1
	v_add3_u32 v3, v3, v4, s90
	ds_write_b16_d16_hi v2, v3 offset:320
	v_sub_f32_e32 v3, v94, v0
	v_mul_f32_e32 v3, v3, v1
	v_bfe_u32 v4, v3, 16, 1
	v_add3_u32 v3, v3, v4, s90
	v_sub_f32_e32 v0, v78, v0
	ds_write_b16_d16_hi v2, v3 offset:384
	v_mul_f32_e32 v3, v0, v1
	v_pk_add_f32 v[0:1], v[130:131], v[6:7]
	s_nop 0
	v_pk_mul_f32 v[0:1], v[0:1], s[36:37] op_sel_hi:[1,0]
	s_nop 0
	v_fma_f32 v1, -v0, v0, v1
	v_max_f32_e32 v1, 0, v1
	v_add_f32_e32 v1, 0x358637bd, v1
	v_mul_f32_e32 v4, 0x4b800000, v1
	v_cmp_gt_f32_e32 vcc, s89, v1
	s_nop 1
	v_cndmask_b32_e32 v1, v1, v4, vcc
	v_rsq_f32_e32 v1, v1
	v_bfe_u32 v4, v3, 16, 1
	v_add3_u32 v3, v3, v4, s90
	ds_write_b16_d16_hi v2, v3 offset:448
	v_mul_f32_e32 v2, 0x45800000, v1
	v_cndmask_b32_e32 v1, v1, v2, vcc
	v_sub_f32_e32 v3, v31, v0
	v_mul_f32_e32 v3, v3, v1
	v_lshlrev_b32_e32 v2, 10, v160
	v_bfe_u32 v4, v3, 16, 1
	v_add3_u32 v3, v3, v4, s90
	v_add3_u32 v2, 0, v2, v16
	ds_write_b16_d16_hi v2, v3
	v_sub_f32_e32 v3, v15, v0
	v_mul_f32_e32 v3, v3, v1
	v_bfe_u32 v4, v3, 16, 1
	v_add3_u32 v3, v3, v4, s90
	ds_write_b16_d16_hi v2, v3 offset:64
	v_sub_f32_e32 v3, v47, v0
	v_mul_f32_e32 v3, v3, v1
	v_bfe_u32 v4, v3, 16, 1
	v_add3_u32 v3, v3, v4, s90
	ds_write_b16_d16_hi v2, v3 offset:128
	v_sub_f32_e32 v3, v63, v0
	v_mul_f32_e32 v3, v3, v1
	v_bfe_u32 v4, v3, 16, 1
	v_add3_u32 v3, v3, v4, s90
	ds_write_b16_d16_hi v2, v3 offset:192
	v_sub_f32_e32 v3, v111, v0
	v_mul_f32_e32 v3, v3, v1
	v_bfe_u32 v4, v3, 16, 1
	v_add3_u32 v3, v3, v4, s90
	ds_write_b16_d16_hi v2, v3 offset:256
	v_sub_f32_e32 v3, v127, v0
	v_mul_f32_e32 v3, v3, v1
	v_bfe_u32 v4, v3, 16, 1
	v_add3_u32 v3, v3, v4, s90
	ds_write_b16_d16_hi v2, v3 offset:320
	v_sub_f32_e32 v3, v95, v0
	v_sub_f32_e32 v0, v79, v0
	v_mul_f32_e32 v3, v3, v1
	v_mul_f32_e32 v0, v0, v1
	v_bfe_u32 v4, v3, 16, 1
	v_bfe_u32 v1, v0, 16, 1
	v_add3_u32 v3, v3, v4, s90
	v_add3_u32 v0, v0, v1, s90
	v_cmp_gt_i32_e32 vcc, s88, v232
	ds_write_b16_d16_hi v2, v3 offset:384
	ds_write_b16_d16_hi v2, v0 offset:448
	s_waitcnt lgkmcnt(0)
	s_barrier
	s_and_saveexec_b64 s[38:39], vcc
	s_cbranch_execz .LBB0_1826
	s_lshl_b32 s4, s8, 2
	s_add_u32 s40, s24, s4
	s_addc_u32 s41, s25, 0
	s_lshl_b64 s[2:3], s[2:3], 11
	s_add_u32 s4, s53, s2
	s_addc_u32 s5, s54, s3
	s_add_u32 s42, s4, s8
	s_addc_u32 s43, s5, 0
	s_add_u32 s2, s55, s2
	s_addc_u32 s3, s56, s3
	s_add_u32 s44, s2, s8
	s_addc_u32 s45, s3, 0
	v_lshl_add_u32 v4, v232, 4, 0
	v_lshlrev_b32_e32 v5, 3, v232
	s_mov_b64 s[46:47], 0
	v_and_b32_e32 v6, 63, v232
	v_lshrrev_b32_e32 v7, 6, v232
	v_lshlrev_b32_e32 v8, 5, v6
	v_lshlrev_b32_e32 v5, 3, v6
	v_lshl_add_u32 v5, v7, 11, v5
	ds_read_b128 v[0:3], v4
	v_add_u32_e32 v4, 0x2000, v4
	global_load_dwordx4 v[40:43], v8, s[40:41]
	global_load_dwordx4 v[44:47], v8, s[40:41] offset:16
	global_load_dwordx2 v[30:31], v5, s[42:43]
	v_add_u32_e32 v22, 0x4000, v5
	s_nop 0
	global_load_dwordx2 v[6:7], v22, s[42:43]
	v_add_u32_e32 v22, 0x4000, v22
	v_mov_b32_e32 v162, v163
	s_movk_i32 s46, 8
	s_waitcnt vmcnt(1)
.Ldloop0:
	s_waitcnt vmcnt(2) lgkmcnt(0)
	v_lshlrev_b32_e32 v10, 16, v0
	v_and_b32_e32 v11, 0xffff0000, v0
	v_lshlrev_b32_e32 v12, 16, v1
	v_and_b32_e32 v13, 0xffff0000, v1
	v_lshlrev_b32_e32 v14, 16, v2
	v_and_b32_e32 v15, 0xffff0000, v2
	v_lshlrev_b32_e32 v16, 16, v3
	v_and_b32_e32 v17, 0xffff0000, v3
	v_cvt_pk_f32_fp8_e32 v[32:33], v30
	v_cvt_pk_f32_fp8_sdwa v[34:35], v30 src0_sel:WORD_1
	v_cvt_pk_f32_fp8_e32 v[36:37], v31
	v_cvt_pk_f32_fp8_sdwa v[38:39], v31 src0_sel:WORD_1
	ds_read_b128 v[0:3], v4
	v_add_u32_e32 v4, 0x2000, v4
	s_cmp_eq_u32 s46, 1
	s_cbranch_scc1 .Ldloop0a
	global_load_dwordx2 v[30:31], v22, s[42:43]
	v_add_u32_e32 v22, 0x4000, v22
; #define LAS __attribute__((address_space(3)))
; __device__ __forceinline__ float sigmoidf_(float x) { return 1.f / (1.f + __expf(-x)); }
; __device__ __forceinline__ float siluf_(float x) { return x / (1.f + __expf(-x)); }
; template <int DK, int DV, bool MLSTM>
; __device__ __forceinline__ void out_unit2(LAS unsigned char* lds, LAS unsigned char* ldstab, const OutArgs a, const int wv) {
;     ...
; #pragma unroll 1
;     for (int id = tid; id < 128 * CPR; id += 512) { const int row = id / CPR, ch = id % CPR;
;         const u32x4 y = *(const LAS u32x4*)(lds + row * TP + ch * 16);
;         const f32x4 g0 = *(const f32x4*)(a.gain + 8 * ch), g1 = *(const f32x4*)(a.gain + 8 * ch + 4);
;         float yv[8] = {bf_lo(y.x), bf_hi(y.x), bf_lo(y.y), bf_hi(y.y), bf_lo(y.z), bf_hi(y.z), bf_lo(y.w), bf_hi(y.w)};
;         float gv[8];
;         if (MLSTM) { const u32x4 g = *(const u32x4*)(a.G + (size_t)row * a.ldg + 8 * ch);
;             gv[0] = bf_lo(g.x); gv[1] = bf_hi(g.x); gv[2] = bf_lo(g.y); gv[3] = bf_hi(g.y); gv[4] = bf_lo(g.z); gv[5] = bf_hi(g.z); gv[6] = bf_lo(g.w); gv[7] = bf_hi(g.w); }
;         else { const u32x2 g = *(const u32x2*)(a.G8 + (size_t)row * a.ldg8 + 8 * ch);
;             const f32x2 e0 = __builtin_amdgcn_cvt_pk_f32_fp8((int)g.x, false), e1 = __builtin_amdgcn_cvt_pk_f32_fp8((int)g.x, true), e2 = __builtin_amdgcn_cvt_pk_f32_fp8((int)g.y, false), e3 = __builtin_amdgcn_cvt_pk_f32_fp8((int)g.y, true);
;             gv[0] = e0[0] * a.g8inv; gv[1] = e0[1] * a.g8inv; gv[2] = e1[0] * a.g8inv; gv[3] = e1[1] * a.g8inv; gv[4] = e2[0] * a.g8inv; gv[5] = e2[1] * a.g8inv; gv[6] = e3[0] * a.g8inv; gv[7] = e3[1] * a.g8inv; }
;         float gn[8] = {g0[0], g0[1], g0[2], g0[3], g1[0], g1[1], g1[2], g1[3]};
;         float ov[8];
; #pragma unroll
;         for (int i = 0; i < 8; ++i) ov[i] = yv[i] * gn[i] * (MLSTM ? sigmoidf_(gv[i]) : siluf_(gv[i]));
;         u32x2 w; w.x = pg8::pk4_fp8c(ov[0] * a.oscale, ov[1] * a.oscale, ov[2] * a.oscale, ov[3] * a.oscale); w.y = pg8::pk4_fp8c(ov[4] * a.oscale, ov[5] * a.oscale, ov[6] * a.oscale, ov[7] * a.oscale);
;         *(u32x2*)(a.Out + (size_t)row * a.ldo + 8 * ch) = w; }
.Ldloop0a:
	v_pk_mul_f32 v[10:11], v[40:41], v[10:11]
	v_pk_mul_f32 v[12:13], v[42:43], v[12:13]
	v_pk_mul_f32 v[14:15], v[44:45], v[14:15]
	v_pk_mul_f32 v[16:17], v[46:47], v[16:17]
	v_pk_mul_f32 v[32:33], v[32:33], v[162:163]
	v_pk_mul_f32 v[34:35], v[34:35], v[162:163]
	v_pk_mul_f32 v[36:37], v[36:37], v[162:163]
	v_pk_mul_f32 v[38:39], v[38:39], v[162:163]
	v_mul_f32_e32 v48, 0xbfb8aa3b, v32
	v_mul_f32_e32 v49, 0xbfb8aa3b, v33
	v_mul_f32_e32 v50, 0xbfb8aa3b, v34
	v_mul_f32_e32 v51, 0xbfb8aa3b, v35
	v_mul_f32_e32 v52, 0xbfb8aa3b, v36
	v_mul_f32_e32 v53, 0xbfb8aa3b, v37
	v_mul_f32_e32 v54, 0xbfb8aa3b, v38
	v_mul_f32_e32 v55, 0xbfb8aa3b, v39
	v_exp_f32_e32 v48, v48
	v_exp_f32_e32 v49, v49
	v_exp_f32_e32 v50, v50
	v_exp_f32_e32 v51, v51
	v_exp_f32_e32 v52, v52
	v_exp_f32_e32 v53, v53
	v_exp_f32_e32 v54, v54
	v_exp_f32_e32 v55, v55
	v_add_f32_e32 v48, 1.0, v48
	v_add_f32_e32 v49, 1.0, v49
	v_add_f32_e32 v50, 1.0, v50
	v_add_f32_e32 v51, 1.0, v51
	v_add_f32_e32 v52, 1.0, v52
	v_add_f32_e32 v53, 1.0, v53
	v_add_f32_e32 v54, 1.0, v54
	v_add_f32_e32 v55, 1.0, v55
	v_rcp_f32_e32 v56, v48
	v_rcp_f32_e32 v57, v49
	v_rcp_f32_e32 v58, v50
	v_rcp_f32_e32 v59, v51
	v_rcp_f32_e32 v60, v52
	v_rcp_f32_e32 v61, v53
	v_rcp_f32_e32 v62, v54
	v_rcp_f32_e32 v63, v55
	v_fma_f32 v8, -v48, v56, 1.0
	v_fma_f32 v9, -v49, v57, 1.0
	v_fma_f32 v18, -v50, v58, 1.0
	v_fma_f32 v19, -v51, v59, 1.0
	v_fma_f32 v20, -v52, v60, 1.0
	v_fma_f32 v21, -v53, v61, 1.0
	v_fma_f32 v23, -v54, v62, 1.0
	v_fma_f32 v26, -v55, v63, 1.0
	v_fmac_f32_e32 v56, v8, v56
	v_fmac_f32_e32 v57, v9, v57
	v_fmac_f32_e32 v58, v18, v58
	v_fmac_f32_e32 v59, v19, v59
	v_fmac_f32_e32 v60, v20, v60
	v_fmac_f32_e32 v61, v21, v61
	v_fmac_f32_e32 v62, v23, v62
	v_fmac_f32_e32 v63, v26, v63
	v_mul_f32_e32 v64, v32, v56
	v_mul_f32_e32 v65, v33, v57
	v_mul_f32_e32 v66, v34, v58
	v_mul_f32_e32 v67, v35, v59
	v_mul_f32_e32 v68, v36, v60
	v_mul_f32_e32 v69, v37, v61
	v_mul_f32_e32 v70, v38, v62
	v_mul_f32_e32 v71, v39, v63
	v_fma_f32 v8, -v48, v64, v32
	v_fma_f32 v9, -v49, v65, v33
	v_fma_f32 v18, -v50, v66, v34
	v_fma_f32 v19, -v51, v67, v35
	v_fma_f32 v20, -v52, v68, v36
	v_fma_f32 v21, -v53, v69, v37
	v_fma_f32 v23, -v54, v70, v38
	v_fma_f32 v26, -v55, v71, v39
	v_fmac_f32_e32 v64, v8, v56
	v_fmac_f32_e32 v65, v9, v57
	v_fmac_f32_e32 v66, v18, v58
	v_fmac_f32_e32 v67, v19, v59
	v_fmac_f32_e32 v68, v20, v60
	v_fmac_f32_e32 v69, v21, v61
	v_fmac_f32_e32 v70, v23, v62
	v_fmac_f32_e32 v71, v26, v63
	v_fma_f32 v8, -v48, v64, v32
	v_fma_f32 v9, -v49, v65, v33
	v_fma_f32 v18, -v50, v66, v34
	v_fma_f32 v19, -v51, v67, v35
	v_fma_f32 v20, -v52, v68, v36
	v_fma_f32 v21, -v53, v69, v37
	v_fma_f32 v23, -v54, v70, v38
	v_fma_f32 v26, -v55, v71, v39
	v_fma_f32 v8, v8, v56, v64
	v_fma_f32 v9, v9, v57, v65
	v_fma_f32 v18, v18, v58, v66
	v_fma_f32 v19, v19, v59, v67
	v_fma_f32 v20, v20, v60, v68
	v_fma_f32 v21, v21, v61, v69
	v_fma_f32 v23, v23, v62, v70
	v_fma_f32 v26, v26, v63, v71
	v_div_fixup_f32 v8, v8, v48, v32
	v_div_fixup_f32 v9, v9, v49, v33
	v_div_fixup_f32 v18, v18, v50, v34
	v_div_fixup_f32 v19, v19, v51, v35
	v_div_fixup_f32 v20, v20, v52, v36
	v_div_fixup_f32 v21, v21, v53, v37
	v_div_fixup_f32 v23, v23, v54, v38
	v_div_fixup_f32 v26, v26, v55, v39
	v_mul_f32_e32 v10, v10, v8
	v_mul_f32_e32 v11, v11, v9
	v_mul_f32_e32 v12, v12, v18
	v_mul_f32_e32 v13, v13, v19
	v_mul_f32_e32 v14, v14, v20
	v_mul_f32_e32 v15, v15, v21
	v_mul_f32_e32 v16, v16, v23
	v_mul_f32_e32 v17, v17, v26
	v_mul_f32_e32 v10, 0x41800000, v10
	v_mul_f32_e32 v11, 0x41800000, v11
	v_mul_f32_e32 v12, 0x41800000, v12
	v_mul_f32_e32 v13, 0x41800000, v13
	v_mul_f32_e32 v14, 0x41800000, v14
	v_mul_f32_e32 v15, 0x41800000, v15
	v_mul_f32_e32 v16, 0x41800000, v16
	v_mul_f32_e32 v17, 0x41800000, v17
	v_med3_f32 v10, v10, s91, v231
	v_med3_f32 v11, v11, s91, v231
	v_med3_f32 v12, v12, s91, v231
	v_med3_f32 v13, v13, s91, v231
	v_med3_f32 v14, v14, s91, v231
	v_med3_f32 v15, v15, s91, v231
	v_med3_f32 v16, v16, s91, v231
	v_med3_f32 v17, v17, s91, v231
	v_cvt_pk_fp8_f32 v24, v10, v11
	v_cvt_pk_fp8_f32 v25, v14, v15
	s_nop 0
	v_cvt_pk_fp8_f32 v24, v12, v13 op_sel:[0,0,1]
	v_cvt_pk_fp8_f32 v25, v16, v17 op_sel:[0,0,1]
	s_nop 0
	global_store_dwordx2 v5, v[24:25], s[44:45]
	v_add_u32_e32 v5, 0x4000, v5
	s_waitcnt vmcnt(2) lgkmcnt(0)
	v_lshlrev_b32_e32 v10, 16, v0
	v_and_b32_e32 v11, 0xffff0000, v0
	v_lshlrev_b32_e32 v12, 16, v1
	v_and_b32_e32 v13, 0xffff0000, v1
	v_lshlrev_b32_e32 v14, 16, v2
	v_and_b32_e32 v15, 0xffff0000, v2
	v_lshlrev_b32_e32 v16, 16, v3
	v_and_b32_e32 v17, 0xffff0000, v3
	v_cvt_pk_f32_fp8_e32 v[32:33], v6
	v_cvt_pk_f32_fp8_sdwa v[34:35], v6 src0_sel:WORD_1
	v_cvt_pk_f32_fp8_e32 v[36:37], v7
	v_cvt_pk_f32_fp8_sdwa v[38:39], v7 src0_sel:WORD_1
	ds_read_b128 v[0:3], v4
	v_add_u32_e32 v4, 0x2000, v4
	s_cmp_eq_u32 s46, 1
	s_cbranch_scc1 .Ldloop0b
	global_load_dwordx2 v[6:7], v22, s[42:43]
	v_add_u32_e32 v22, 0x4000, v22
; #define LAS __attribute__((address_space(3)))
; __device__ __forceinline__ float sigmoidf_(float x) { return 1.f / (1.f + __expf(-x)); }
; __device__ __forceinline__ float siluf_(float x) { return x / (1.f + __expf(-x)); }
; template <int DK, int DV, bool MLSTM>
; __device__ __forceinline__ void out_unit2(LAS unsigned char* lds, LAS unsigned char* ldstab, const OutArgs a, const int wv) {
;     ...
; #pragma unroll 1
;     for (int id = tid; id < 128 * CPR; id += 512) { const int row = id / CPR, ch = id % CPR;
;         const u32x4 y = *(const LAS u32x4*)(lds + row * TP + ch * 16);
;         const f32x4 g0 = *(const f32x4*)(a.gain + 8 * ch), g1 = *(const f32x4*)(a.gain + 8 * ch + 4);
;         float yv[8] = {bf_lo(y.x), bf_hi(y.x), bf_lo(y.y), bf_hi(y.y), bf_lo(y.z), bf_hi(y.z), bf_lo(y.w), bf_hi(y.w)};
;         float gv[8];
;         if (MLSTM) { const u32x4 g = *(const u32x4*)(a.G + (size_t)row * a.ldg + 8 * ch);
;             gv[0] = bf_lo(g.x); gv[1] = bf_hi(g.x); gv[2] = bf_lo(g.y); gv[3] = bf_hi(g.y); gv[4] = bf_lo(g.z); gv[5] = bf_hi(g.z); gv[6] = bf_lo(g.w); gv[7] = bf_hi(g.w); }
;         else { const u32x2 g = *(const u32x2*)(a.G8 + (size_t)row * a.ldg8 + 8 * ch);
;             const f32x2 e0 = __builtin_amdgcn_cvt_pk_f32_fp8((int)g.x, false), e1 = __builtin_amdgcn_cvt_pk_f32_fp8((int)g.x, true), e2 = __builtin_amdgcn_cvt_pk_f32_fp8((int)g.y, false), e3 = __builtin_amdgcn_cvt_pk_f32_fp8((int)g.y, true);
;             gv[0] = e0[0] * a.g8inv; gv[1] = e0[1] * a.g8inv; gv[2] = e1[0] * a.g8inv; gv[3] = e1[1] * a.g8inv; gv[4] = e2[0] * a.g8inv; gv[5] = e2[1] * a.g8inv; gv[6] = e3[0] * a.g8inv; gv[7] = e3[1] * a.g8inv; }
;         float gn[8] = {g0[0], g0[1], g0[2], g0[3], g1[0], g1[1], g1[2], g1[3]};
;         float ov[8];
; #pragma unroll
;         for (int i = 0; i < 8; ++i) ov[i] = yv[i] * gn[i] * (MLSTM ? sigmoidf_(gv[i]) : siluf_(gv[i]));
;         u32x2 w; w.x = pg8::pk4_fp8c(ov[0] * a.oscale, ov[1] * a.oscale, ov[2] * a.oscale, ov[3] * a.oscale); w.y = pg8::pk4_fp8c(ov[4] * a.oscale, ov[5] * a.oscale, ov[6] * a.oscale, ov[7] * a.oscale);
;         *(u32x2*)(a.Out + (size_t)row * a.ldo + 8 * ch) = w; }
.Ldloop0b:
	v_pk_mul_f32 v[10:11], v[40:41], v[10:11]
	v_pk_mul_f32 v[12:13], v[42:43], v[12:13]
	v_pk_mul_f32 v[14:15], v[44:45], v[14:15]
	v_pk_mul_f32 v[16:17], v[46:47], v[16:17]
	v_pk_mul_f32 v[32:33], v[32:33], v[162:163]
	v_pk_mul_f32 v[34:35], v[34:35], v[162:163]
	v_pk_mul_f32 v[36:37], v[36:37], v[162:163]
	v_pk_mul_f32 v[38:39], v[38:39], v[162:163]
	v_mul_f32_e32 v48, 0xbfb8aa3b, v32
	v_mul_f32_e32 v49, 0xbfb8aa3b, v33
	v_mul_f32_e32 v50, 0xbfb8aa3b, v34
	v_mul_f32_e32 v51, 0xbfb8aa3b, v35
	v_mul_f32_e32 v52, 0xbfb8aa3b, v36
	v_mul_f32_e32 v53, 0xbfb8aa3b, v37
	v_mul_f32_e32 v54, 0xbfb8aa3b, v38
	v_mul_f32_e32 v55, 0xbfb8aa3b, v39
	v_exp_f32_e32 v48, v48
	v_exp_f32_e32 v49, v49
	v_exp_f32_e32 v50, v50
	v_exp_f32_e32 v51, v51
	v_exp_f32_e32 v52, v52
	v_exp_f32_e32 v53, v53
	v_exp_f32_e32 v54, v54
	v_exp_f32_e32 v55, v55
	v_add_f32_e32 v48, 1.0, v48
	v_add_f32_e32 v49, 1.0, v49
	v_add_f32_e32 v50, 1.0, v50
	v_add_f32_e32 v51, 1.0, v51
	v_add_f32_e32 v52, 1.0, v52
	v_add_f32_e32 v53, 1.0, v53
	v_add_f32_e32 v54, 1.0, v54
	v_add_f32_e32 v55, 1.0, v55
	v_rcp_f32_e32 v56, v48
	v_rcp_f32_e32 v57, v49
	v_rcp_f32_e32 v58, v50
	v_rcp_f32_e32 v59, v51
	v_rcp_f32_e32 v60, v52
	v_rcp_f32_e32 v61, v53
	v_rcp_f32_e32 v62, v54
	v_rcp_f32_e32 v63, v55
	v_fma_f32 v8, -v48, v56, 1.0
	v_fma_f32 v9, -v49, v57, 1.0
	v_fma_f32 v18, -v50, v58, 1.0
	v_fma_f32 v19, -v51, v59, 1.0
	v_fma_f32 v20, -v52, v60, 1.0
	v_fma_f32 v21, -v53, v61, 1.0
	v_fma_f32 v23, -v54, v62, 1.0
	v_fma_f32 v26, -v55, v63, 1.0
	v_fmac_f32_e32 v56, v8, v56
	v_fmac_f32_e32 v57, v9, v57
	v_fmac_f32_e32 v58, v18, v58
	v_fmac_f32_e32 v59, v19, v59
	v_fmac_f32_e32 v60, v20, v60
	v_fmac_f32_e32 v61, v21, v61
	v_fmac_f32_e32 v62, v23, v62
	v_fmac_f32_e32 v63, v26, v63
	v_mul_f32_e32 v64, v32, v56
	v_mul_f32_e32 v65, v33, v57
	v_mul_f32_e32 v66, v34, v58
	v_mul_f32_e32 v67, v35, v59
	v_mul_f32_e32 v68, v36, v60
	v_mul_f32_e32 v69, v37, v61
	v_mul_f32_e32 v70, v38, v62
	v_mul_f32_e32 v71, v39, v63
	v_fma_f32 v8, -v48, v64, v32
	v_fma_f32 v9, -v49, v65, v33
	v_fma_f32 v18, -v50, v66, v34
	v_fma_f32 v19, -v51, v67, v35
	v_fma_f32 v20, -v52, v68, v36
	v_fma_f32 v21, -v53, v69, v37
	v_fma_f32 v23, -v54, v70, v38
	v_fma_f32 v26, -v55, v71, v39
	v_fmac_f32_e32 v64, v8, v56
	v_fmac_f32_e32 v65, v9, v57
	v_fmac_f32_e32 v66, v18, v58
	v_fmac_f32_e32 v67, v19, v59
	v_fmac_f32_e32 v68, v20, v60
	v_fmac_f32_e32 v69, v21, v61
	v_fmac_f32_e32 v70, v23, v62
	v_fmac_f32_e32 v71, v26, v63
	v_fma_f32 v8, -v48, v64, v32
	v_fma_f32 v9, -v49, v65, v33
	v_fma_f32 v18, -v50, v66, v34
	v_fma_f32 v19, -v51, v67, v35
	v_fma_f32 v20, -v52, v68, v36
	v_fma_f32 v21, -v53, v69, v37
	v_fma_f32 v23, -v54, v70, v38
	v_fma_f32 v26, -v55, v71, v39
	v_fma_f32 v8, v8, v56, v64
	v_fma_f32 v9, v9, v57, v65
	v_fma_f32 v18, v18, v58, v66
	v_fma_f32 v19, v19, v59, v67
	v_fma_f32 v20, v20, v60, v68
	v_fma_f32 v21, v21, v61, v69
	v_fma_f32 v23, v23, v62, v70
	v_fma_f32 v26, v26, v63, v71
	v_div_fixup_f32 v8, v8, v48, v32
	v_div_fixup_f32 v9, v9, v49, v33
	v_div_fixup_f32 v18, v18, v50, v34
	v_div_fixup_f32 v19, v19, v51, v35
	v_div_fixup_f32 v20, v20, v52, v36
	v_div_fixup_f32 v21, v21, v53, v37
	v_div_fixup_f32 v23, v23, v54, v38
	v_div_fixup_f32 v26, v26, v55, v39
	v_mul_f32_e32 v10, v10, v8
	v_mul_f32_e32 v11, v11, v9
	v_mul_f32_e32 v12, v12, v18
	v_mul_f32_e32 v13, v13, v19
	v_mul_f32_e32 v14, v14, v20
	v_mul_f32_e32 v15, v15, v21
	v_mul_f32_e32 v16, v16, v23
	v_mul_f32_e32 v17, v17, v26
	v_mul_f32_e32 v10, 0x41800000, v10
	v_mul_f32_e32 v11, 0x41800000, v11
	v_mul_f32_e32 v12, 0x41800000, v12
	v_mul_f32_e32 v13, 0x41800000, v13
	v_mul_f32_e32 v14, 0x41800000, v14
	v_mul_f32_e32 v15, 0x41800000, v15
	v_mul_f32_e32 v16, 0x41800000, v16
	v_mul_f32_e32 v17, 0x41800000, v17
	v_med3_f32 v10, v10, s91, v231
	v_med3_f32 v11, v11, s91, v231
	v_med3_f32 v12, v12, s91, v231
	v_med3_f32 v13, v13, s91, v231
	v_med3_f32 v14, v14, s91, v231
	v_med3_f32 v15, v15, s91, v231
	v_med3_f32 v16, v16, s91, v231
	v_med3_f32 v17, v17, s91, v231
	v_cvt_pk_fp8_f32 v24, v10, v11
	v_cvt_pk_fp8_f32 v25, v14, v15
	s_nop 0
	v_cvt_pk_fp8_f32 v24, v12, v13 op_sel:[0,0,1]
	v_cvt_pk_fp8_f32 v25, v16, v17 op_sel:[0,0,1]
	s_nop 0
	global_store_dwordx2 v5, v[24:25], s[44:45]
	v_add_u32_e32 v5, 0x4000, v5
	s_add_i32 s46, s46, -1
	s_cmp_lg_u32 s46, 0
	s_cbranch_scc1 .Ldloop0
	s_waitcnt lgkmcnt(0)
	s_branch .LBB0_1826

; #define LAS __attribute__((address_space(3)))
; __device__ __forceinline__ bf16_t f2bf(float f) { unsigned u = __builtin_bit_cast(unsigned, f); return (bf16_t)((u + 0x7fffu + ((u >> 16) & 1u)) >> 16); }
; __device__ __forceinline__ int crow(int r, int hi) { return (r & 3) + 8 * (r >> 2) + 4 * hi; }
; __device__ __forceinline__ int crow(int r, int hi) { return (r & 3) + 8 * (r >> 2) + 4 * hi; }
; template <int DK, int DV, bool MLSTM>
; __device__ __forceinline__ void out_unit2(LAS unsigned char* lds, LAS unsigned char* ldstab, const OutArgs a, const int wv) {
;     ...
;     __syncthreads();
;     constexpr int TP = DV * 2;
;     static_assert(128 * TP <= 2 * NPK * 32768, "output tile fits the Q + K regions");
; #pragma unroll
;     for (int r = 0; r < 16; ++r) {
;         const int row = 32 * rb + crow(r, hi);
;         const float t1 = s1[r] + exch[((1 - dh) * 128 + row) * 2], t2 = s2[r] + exch[((1 - dh) * 128 + row) * 2 + 1];
;         float mean, inv;
;         if (MLSTM) { mean = 0.f; inv = rsqrtf(t2 * (1.f / DV) + EPS); }
;         else { mean = t1 * (1.f / DV); inv = rsqrtf(fmaxf(t2 * (1.f / DV) - mean * mean, 0.f) + EPS); }
; #pragma unroll
;         for (int nb = 0; nb < NB; ++nb) { const int col = dh * (DV / 2) + 32 * nb + r32;
;             *(LAS bf16_t*)(lds + row * TP + col * 2) = f2bf((o[nb][r] - mean) * inv); }
.LBB0_4313:
	s_or_b64 exec, exec, s[4:5]
	v_lshlrev_b32_e32 v164, 1, v219
	v_subrev_u32_e32 v164, s6, v164
	s_add_i32 s4, 0, 0x22100
	v_lshl_add_u32 v164, v164, 2, s4
	s_waitcnt vmcnt(0) lgkmcnt(0)
	s_barrier
	ds_read_b128 v[164:167], v164 offset:1024
	v_lshlrev_b32_e32 v168, 1, v217
	v_subrev_u32_e32 v168, s6, v168
	v_lshl_add_u32 v168, v168, 2, s4
	ds_read2_b64 v[168:171], v168 offset0:128 offset1:129
	s_waitcnt lgkmcnt(1)
	v_pk_add_f32 v[156:157], v[156:157], v[164:165]
	s_nop 0
	v_pk_mul_f32 v[156:157], v[156:157], s[26:27] op_sel_hi:[1,0]
	s_nop 0
	v_fma_f32 v157, -v156, v156, v157
	v_max_f32_e32 v157, 0, v157
	v_add_f32_e32 v157, 0x358637bd, v157
	v_mul_f32_e32 v164, 0x4b800000, v157
	v_cmp_gt_f32_e32 vcc, s89, v157
	v_sub_f32_e32 v16, v16, v156
	v_sub_f32_e32 v0, v0, v156
	v_cndmask_b32_e32 v157, v157, v164, vcc
	v_rsq_f32_e32 v157, v157
	v_or_b32_e32 v164, s6, v233
	v_mul_f32_e32 v165, 0x45800000, v157
	v_cndmask_b32_e32 v157, v157, v165, vcc
	v_mul_f32_e32 v16, v16, v157
	v_bfe_u32 v172, v16, 16, 1
	v_lshlrev_b32_e32 v165, 10, v219
	v_add3_u32 v172, v16, v172, s90
	v_lshlrev_b32_e32 v16, 1, v164
	v_mul_f32_e32 v0, v0, v157
	v_add3_u32 v164, 0, v165, v16
	v_bfe_u32 v165, v0, 16, 1
	v_add3_u32 v0, v0, v165, s90
	ds_write_b16_d16_hi v164, v0 offset:64
	v_sub_f32_e32 v0, v32, v156
	v_mul_f32_e32 v0, v0, v157
	v_bfe_u32 v32, v0, 16, 1
	v_add3_u32 v0, v0, v32, s90
	ds_write_b16_d16_hi v164, v0 offset:128
	v_sub_f32_e32 v0, v48, v156
	v_mul_f32_e32 v0, v0, v157
	v_bfe_u32 v32, v0, 16, 1
	v_add3_u32 v0, v0, v32, s90
	ds_write_b16_d16_hi v164, v0 offset:192
	v_sub_f32_e32 v0, v96, v156
	v_mul_f32_e32 v0, v0, v157
	v_bfe_u32 v32, v0, 16, 1
	v_add3_u32 v0, v0, v32, s90
	ds_write_b16_d16_hi v164, v0 offset:256
	v_sub_f32_e32 v0, v112, v156
	v_mul_f32_e32 v0, v0, v157
	v_bfe_u32 v32, v0, 16, 1
	v_add3_u32 v0, v0, v32, s90
	ds_write_b16_d16_hi v164, v0 offset:320
	v_sub_f32_e32 v0, v80, v156
	v_mul_f32_e32 v0, v0, v157
	v_bfe_u32 v32, v0, 16, 1
	v_add3_u32 v0, v0, v32, s90
	ds_write_b16_d16_hi v164, v0 offset:384
	v_sub_f32_e32 v0, v64, v156
	v_mul_f32_e32 v0, v0, v157
	v_pk_add_f32 v[156:157], v[158:159], v[166:167]
	ds_write_b16_d16_hi v164, v172
	v_pk_mul_f32 v[156:157], v[156:157], s[26:27] op_sel_hi:[1,0]
	s_nop 0
	v_fma_f32 v32, -v156, v156, v157
	v_max_f32_e32 v32, 0, v32
	v_add_f32_e32 v32, 0x358637bd, v32
	v_mul_f32_e32 v48, 0x4b800000, v32
	v_cmp_gt_f32_e32 vcc, s89, v32
	v_sub_f32_e32 v17, v17, v156
	v_sub_f32_e32 v1, v1, v156
	v_cndmask_b32_e32 v32, v32, v48, vcc
	v_rsq_f32_e32 v32, v32
	v_bfe_u32 v48, v0, 16, 1
	v_add3_u32 v0, v0, v48, s90
	ds_write_b16_d16_hi v164, v0 offset:448
	v_mul_f32_e32 v0, 0x45800000, v32
	v_cndmask_b32_e32 v0, v32, v0, vcc
	v_mul_f32_e32 v17, v17, v0
	v_lshlrev_b32_e32 v32, 10, v218
	v_bfe_u32 v48, v17, 16, 1
	v_add3_u32 v17, v17, v48, s90
	v_add3_u32 v32, 0, v32, v16
	v_mul_f32_e32 v1, v1, v0
	ds_write_b16_d16_hi v32, v17
	v_bfe_u32 v17, v1, 16, 1
	v_add3_u32 v1, v1, v17, s90
	ds_write_b16_d16_hi v32, v1 offset:64
	v_sub_f32_e32 v1, v33, v156
	v_mul_f32_e32 v1, v1, v0
	v_bfe_u32 v17, v1, 16, 1
	v_add3_u32 v1, v1, v17, s90
	ds_write_b16_d16_hi v32, v1 offset:128
	v_sub_f32_e32 v1, v49, v156
	v_mul_f32_e32 v1, v1, v0
	v_bfe_u32 v17, v1, 16, 1
	v_add3_u32 v1, v1, v17, s90
	ds_write_b16_d16_hi v32, v1 offset:192
	v_sub_f32_e32 v1, v97, v156
	v_mul_f32_e32 v1, v1, v0
	v_bfe_u32 v17, v1, 16, 1
	v_add3_u32 v1, v1, v17, s90
	ds_write_b16_d16_hi v32, v1 offset:256
	v_sub_f32_e32 v1, v113, v156
	v_mul_f32_e32 v1, v1, v0
	v_bfe_u32 v17, v1, 16, 1
	v_add3_u32 v1, v1, v17, s90
	ds_write_b16_d16_hi v32, v1 offset:320
	v_sub_f32_e32 v1, v81, v156
	v_mul_f32_e32 v1, v1, v0
	v_bfe_u32 v17, v1, 16, 1
	v_add3_u32 v1, v1, v17, s90
	ds_write_b16_d16_hi v32, v1 offset:384
	v_sub_f32_e32 v1, v65, v156
	v_mul_f32_e32 v17, v1, v0
	s_waitcnt lgkmcnt(14)
	v_pk_add_f32 v[0:1], v[152:153], v[168:169]
	s_nop 0
	v_pk_mul_f32 v[0:1], v[0:1], s[26:27] op_sel_hi:[1,0]
	s_nop 0
	v_fma_f32 v1, -v0, v0, v1
	v_max_f32_e32 v1, 0, v1
	v_add_f32_e32 v1, 0x358637bd, v1
	v_mul_f32_e32 v33, 0x4b800000, v1
	v_cmp_gt_f32_e32 vcc, s89, v1
	v_sub_f32_e32 v18, v18, v0
	v_sub_f32_e32 v2, v2, v0
	v_cndmask_b32_e32 v1, v1, v33, vcc
	v_rsq_f32_e32 v1, v1
	v_bfe_u32 v33, v17, 16, 1
	v_add3_u32 v17, v17, v33, s90
	ds_write_b16_d16_hi v32, v17 offset:448
	v_mul_f32_e32 v17, 0x45800000, v1
	v_cndmask_b32_e32 v1, v1, v17, vcc
	v_mul_f32_e32 v18, v18, v1
	v_lshlrev_b32_e32 v17, 10, v217
	v_bfe_u32 v32, v18, 16, 1
	v_add3_u32 v18, v18, v32, s90
	v_add3_u32 v17, 0, v17, v16
	v_mul_f32_e32 v2, v2, v1
	ds_write_b16_d16_hi v17, v18
	v_bfe_u32 v18, v2, 16, 1
	v_add3_u32 v2, v2, v18, s90
	ds_write_b16_d16_hi v17, v2 offset:64
	v_sub_f32_e32 v2, v34, v0
	v_mul_f32_e32 v2, v2, v1
	v_bfe_u32 v18, v2, 16, 1
	v_add3_u32 v2, v2, v18, s90
	ds_write_b16_d16_hi v17, v2 offset:128
	v_sub_f32_e32 v2, v50, v0
	v_mul_f32_e32 v2, v2, v1
	v_bfe_u32 v18, v2, 16, 1
	v_add3_u32 v2, v2, v18, s90
	ds_write_b16_d16_hi v17, v2 offset:192
	v_sub_f32_e32 v2, v98, v0
	v_mul_f32_e32 v2, v2, v1
	v_bfe_u32 v18, v2, 16, 1
	v_add3_u32 v2, v2, v18, s90
	ds_write_b16_d16_hi v17, v2 offset:256
	v_sub_f32_e32 v2, v114, v0
	v_mul_f32_e32 v2, v2, v1
	v_bfe_u32 v18, v2, 16, 1
	v_add3_u32 v2, v2, v18, s90
	ds_write_b16_d16_hi v17, v2 offset:320
	v_sub_f32_e32 v2, v82, v0
	v_mul_f32_e32 v2, v2, v1
	v_bfe_u32 v18, v2, 16, 1
	v_add3_u32 v2, v2, v18, s90
	v_sub_f32_e32 v0, v66, v0
	ds_write_b16_d16_hi v17, v2 offset:384
	v_mul_f32_e32 v2, v0, v1
	v_pk_add_f32 v[0:1], v[154:155], v[170:171]
	s_nop 0
	v_pk_mul_f32 v[0:1], v[0:1], s[26:27] op_sel_hi:[1,0]
	s_nop 0
	v_fma_f32 v1, -v0, v0, v1
	v_max_f32_e32 v1, 0, v1
; #define LAS __attribute__((address_space(3)))
; __device__ __forceinline__ bf16_t f2bf(float f) { unsigned u = __builtin_bit_cast(unsigned, f); return (bf16_t)((u + 0x7fffu + ((u >> 16) & 1u)) >> 16); }
; __device__ __forceinline__ int crow(int r, int hi) { return (r & 3) + 8 * (r >> 2) + 4 * hi; }
; __device__ __forceinline__ int crow(int r, int hi) { return (r & 3) + 8 * (r >> 2) + 4 * hi; }
; template <int DK, int DV, bool MLSTM>
; __device__ __forceinline__ void out_unit2(LAS unsigned char* lds, LAS unsigned char* ldstab, const OutArgs a, const int wv) {
;     ...
;     for (int r = 0; r < 16; ++r) {
;         const int row = 32 * rb + crow(r, hi);
;         const float t1 = s1[r] + exch[((1 - dh) * 128 + row) * 2], t2 = s2[r] + exch[((1 - dh) * 128 + row) * 2 + 1];
;         float mean, inv;
;         if (MLSTM) { mean = 0.f; inv = rsqrtf(t2 * (1.f / DV) + EPS); }
;         else { mean = t1 * (1.f / DV); inv = rsqrtf(fmaxf(t2 * (1.f / DV) - mean * mean, 0.f) + EPS); }
; #pragma unroll
;         for (int nb = 0; nb < NB; ++nb) { const int col = dh * (DV / 2) + 32 * nb + r32;
;             *(LAS bf16_t*)(lds + row * TP + col * 2) = f2bf((o[nb][r] - mean) * inv); }
	v_add_f32_e32 v1, 0x358637bd, v1
	v_mul_f32_e32 v18, 0x4b800000, v1
	v_cmp_gt_f32_e32 vcc, s89, v1
	s_nop 1
	v_cndmask_b32_e32 v1, v1, v18, vcc
	v_rsq_f32_e32 v1, v1
	v_bfe_u32 v18, v2, 16, 1
	v_add3_u32 v2, v2, v18, s90
	ds_write_b16_d16_hi v17, v2 offset:448
	v_mul_f32_e32 v2, 0x45800000, v1
	v_cndmask_b32_e32 v1, v1, v2, vcc
	v_sub_f32_e32 v17, v19, v0
	v_mul_f32_e32 v17, v17, v1
	v_lshlrev_b32_e32 v2, 10, v216
	v_bfe_u32 v18, v17, 16, 1
	v_add3_u32 v17, v17, v18, s90
	v_add3_u32 v18, 0, v2, v16
	v_sub_f32_e32 v2, v3, v0
	v_mul_f32_e32 v2, v2, v1
	v_bfe_u32 v3, v2, 16, 1
	v_add3_u32 v2, v2, v3, s90
	ds_write_b16_d16_hi v18, v2 offset:64
	v_sub_f32_e32 v2, v35, v0
	v_mul_f32_e32 v2, v2, v1
	v_bfe_u32 v3, v2, 16, 1
	v_add3_u32 v2, v2, v3, s90
	ds_write_b16_d16_hi v18, v2 offset:128
	v_sub_f32_e32 v2, v51, v0
	v_mul_f32_e32 v2, v2, v1
	v_bfe_u32 v3, v2, 16, 1
	v_add3_u32 v2, v2, v3, s90
	ds_write_b16_d16_hi v18, v2 offset:192
	v_sub_f32_e32 v2, v99, v0
	v_mul_f32_e32 v2, v2, v1
	v_bfe_u32 v3, v2, 16, 1
	v_add3_u32 v2, v2, v3, s90
	ds_write_b16_d16_hi v18, v2 offset:256
	v_sub_f32_e32 v2, v115, v0
	v_mul_f32_e32 v2, v2, v1
	v_bfe_u32 v3, v2, 16, 1
	v_add3_u32 v2, v2, v3, s90
	ds_write_b16_d16_hi v18, v2 offset:320
	v_sub_f32_e32 v2, v83, v0
	v_sub_f32_e32 v0, v67, v0
	ds_write_b16_d16_hi v18, v17
	v_mul_f32_e32 v2, v2, v1
	v_mul_f32_e32 v17, v0, v1
	v_lshlrev_b32_e32 v0, 1, v215
	v_bfe_u32 v3, v2, 16, 1
	v_subrev_u32_e32 v0, s6, v0
	v_add3_u32 v2, v2, v3, s90
	v_lshl_add_u32 v0, v0, 2, s4
	ds_write_b16_d16_hi v18, v2 offset:384
	ds_read2_b64 v[0:3], v0 offset0:128 offset1:129
	v_lshlrev_b32_e32 v19, 1, v213
	v_subrev_u32_e32 v19, s6, v19
	v_lshl_add_u32 v19, v19, 2, s4
	ds_read2_b64 v[32:35], v19 offset0:128 offset1:129
	s_waitcnt lgkmcnt(1)
	v_pk_add_f32 v[0:1], v[148:149], v[0:1]
	s_nop 0
	v_pk_mul_f32 v[0:1], v[0:1], s[26:27] op_sel_hi:[1,0]
	s_nop 0
	v_fma_f32 v1, -v0, v0, v1
	v_max_f32_e32 v1, 0, v1
	v_add_f32_e32 v1, 0x358637bd, v1
	v_mul_f32_e32 v19, 0x4b800000, v1
	v_cmp_gt_f32_e32 vcc, s89, v1
	v_sub_f32_e32 v4, v4, v0
	s_nop 0
	v_cndmask_b32_e32 v1, v1, v19, vcc
	v_rsq_f32_e32 v1, v1
	v_bfe_u32 v19, v17, 16, 1
	v_add3_u32 v17, v17, v19, s90
	ds_write_b16_d16_hi v18, v17 offset:448
	v_mul_f32_e32 v17, 0x45800000, v1
	v_cndmask_b32_e32 v1, v1, v17, vcc
	v_sub_f32_e32 v18, v20, v0
	v_mul_f32_e32 v18, v18, v1
	v_lshlrev_b32_e32 v17, 10, v215
	v_bfe_u32 v19, v18, 16, 1
	v_add3_u32 v18, v18, v19, s90
	v_add3_u32 v17, 0, v17, v16
	v_mul_f32_e32 v4, v4, v1
	ds_write_b16_d16_hi v17, v18
	v_bfe_u32 v18, v4, 16, 1
	v_add3_u32 v4, v4, v18, s90
	ds_write_b16_d16_hi v17, v4 offset:64
	v_sub_f32_e32 v4, v36, v0
	v_mul_f32_e32 v4, v4, v1
	v_bfe_u32 v18, v4, 16, 1
	v_add3_u32 v4, v4, v18, s90
	ds_write_b16_d16_hi v17, v4 offset:128
	v_sub_f32_e32 v4, v52, v0
	v_mul_f32_e32 v4, v4, v1
	v_bfe_u32 v18, v4, 16, 1
	v_add3_u32 v4, v4, v18, s90
	ds_write_b16_d16_hi v17, v4 offset:192
	v_sub_f32_e32 v4, v100, v0
	v_mul_f32_e32 v4, v4, v1
	v_bfe_u32 v18, v4, 16, 1
	v_add3_u32 v4, v4, v18, s90
	ds_write_b16_d16_hi v17, v4 offset:256
	v_sub_f32_e32 v4, v116, v0
	v_mul_f32_e32 v4, v4, v1
	v_bfe_u32 v18, v4, 16, 1
	v_add3_u32 v4, v4, v18, s90
	ds_write_b16_d16_hi v17, v4 offset:320
	v_sub_f32_e32 v4, v84, v0
	v_mul_f32_e32 v4, v4, v1
	v_bfe_u32 v18, v4, 16, 1
	v_add3_u32 v4, v4, v18, s90
	v_sub_f32_e32 v0, v68, v0
	ds_write_b16_d16_hi v17, v4 offset:384
	v_mul_f32_e32 v4, v0, v1
	v_pk_add_f32 v[0:1], v[150:151], v[2:3]
	s_nop 0
	v_pk_mul_f32 v[0:1], v[0:1], s[26:27] op_sel_hi:[1,0]
	s_nop 0
	v_fma_f32 v1, -v0, v0, v1
	v_max_f32_e32 v1, 0, v1
	v_add_f32_e32 v1, 0x358637bd, v1
	v_mul_f32_e32 v2, 0x4b800000, v1
	v_cmp_gt_f32_e32 vcc, s89, v1
	v_sub_f32_e32 v3, v21, v0
	s_nop 0
	v_cndmask_b32_e32 v1, v1, v2, vcc
	v_rsq_f32_e32 v1, v1
	v_bfe_u32 v2, v4, 16, 1
	v_add3_u32 v2, v4, v2, s90
	ds_write_b16_d16_hi v17, v2 offset:448
	v_mul_f32_e32 v2, 0x45800000, v1
	v_cndmask_b32_e32 v1, v1, v2, vcc
	v_mul_f32_e32 v3, v3, v1
	v_lshlrev_b32_e32 v2, 10, v214
	v_bfe_u32 v4, v3, 16, 1
	v_add3_u32 v3, v3, v4, s90
	v_add3_u32 v2, 0, v2, v16
	ds_write_b16_d16_hi v2, v3
	v_sub_f32_e32 v3, v5, v0
	v_mul_f32_e32 v3, v3, v1
	v_bfe_u32 v4, v3, 16, 1
	v_add3_u32 v3, v3, v4, s90
	ds_write_b16_d16_hi v2, v3 offset:64
	v_sub_f32_e32 v3, v37, v0
	v_mul_f32_e32 v3, v3, v1
	v_bfe_u32 v4, v3, 16, 1
	v_add3_u32 v3, v3, v4, s90
	ds_write_b16_d16_hi v2, v3 offset:128
	v_sub_f32_e32 v3, v53, v0
	v_mul_f32_e32 v3, v3, v1
	v_bfe_u32 v4, v3, 16, 1
	v_add3_u32 v3, v3, v4, s90
	ds_write_b16_d16_hi v2, v3 offset:192
	v_sub_f32_e32 v3, v101, v0
	v_mul_f32_e32 v3, v3, v1
	v_bfe_u32 v4, v3, 16, 1
	v_add3_u32 v3, v3, v4, s90
	ds_write_b16_d16_hi v2, v3 offset:256
	v_sub_f32_e32 v3, v117, v0
	v_mul_f32_e32 v3, v3, v1
	v_bfe_u32 v4, v3, 16, 1
	v_add3_u32 v3, v3, v4, s90
	ds_write_b16_d16_hi v2, v3 offset:320
	v_sub_f32_e32 v3, v85, v0
	v_mul_f32_e32 v3, v3, v1
	v_bfe_u32 v4, v3, 16, 1
	v_add3_u32 v3, v3, v4, s90
	v_sub_f32_e32 v0, v69, v0
	ds_write_b16_d16_hi v2, v3 offset:384
	v_mul_f32_e32 v3, v0, v1
	s_waitcnt lgkmcnt(14)
; #define LAS __attribute__((address_space(3)))
; __device__ __forceinline__ bf16_t f2bf(float f) { unsigned u = __builtin_bit_cast(unsigned, f); return (bf16_t)((u + 0x7fffu + ((u >> 16) & 1u)) >> 16); }
; __device__ __forceinline__ int crow(int r, int hi) { return (r & 3) + 8 * (r >> 2) + 4 * hi; }
; __device__ __forceinline__ int crow(int r, int hi) { return (r & 3) + 8 * (r >> 2) + 4 * hi; }
; template <int DK, int DV, bool MLSTM>
; __device__ __forceinline__ void out_unit2(LAS unsigned char* lds, LAS unsigned char* ldstab, const OutArgs a, const int wv) {
;     ...
;     for (int r = 0; r < 16; ++r) {
;         const int row = 32 * rb + crow(r, hi);
;         const float t1 = s1[r] + exch[((1 - dh) * 128 + row) * 2], t2 = s2[r] + exch[((1 - dh) * 128 + row) * 2 + 1];
;         float mean, inv;
;         if (MLSTM) { mean = 0.f; inv = rsqrtf(t2 * (1.f / DV) + EPS); }
;         else { mean = t1 * (1.f / DV); inv = rsqrtf(fmaxf(t2 * (1.f / DV) - mean * mean, 0.f) + EPS); }
; #pragma unroll
;         for (int nb = 0; nb < NB; ++nb) { const int col = dh * (DV / 2) + 32 * nb + r32;
;             *(LAS bf16_t*)(lds + row * TP + col * 2) = f2bf((o[nb][r] - mean) * inv); }
	v_pk_add_f32 v[0:1], v[144:145], v[32:33]
	s_nop 0
	v_pk_mul_f32 v[0:1], v[0:1], s[26:27] op_sel_hi:[1,0]
	s_nop 0
	v_fma_f32 v1, -v0, v0, v1
	v_max_f32_e32 v1, 0, v1
	v_add_f32_e32 v1, 0x358637bd, v1
	v_mul_f32_e32 v4, 0x4b800000, v1
	v_cmp_gt_f32_e32 vcc, s89, v1
	s_nop 1
	v_cndmask_b32_e32 v1, v1, v4, vcc
	v_rsq_f32_e32 v1, v1
	v_bfe_u32 v4, v3, 16, 1
	v_add3_u32 v3, v3, v4, s90
	ds_write_b16_d16_hi v2, v3 offset:448
	v_mul_f32_e32 v2, 0x45800000, v1
	v_cndmask_b32_e32 v1, v1, v2, vcc
	v_sub_f32_e32 v3, v22, v0
	v_mul_f32_e32 v3, v3, v1
	v_lshlrev_b32_e32 v2, 10, v213
	v_bfe_u32 v4, v3, 16, 1
	v_add3_u32 v3, v3, v4, s90
	v_add3_u32 v2, 0, v2, v16
	ds_write_b16_d16_hi v2, v3
	v_sub_f32_e32 v3, v6, v0
	v_mul_f32_e32 v3, v3, v1
	v_bfe_u32 v4, v3, 16, 1
	v_add3_u32 v3, v3, v4, s90
	ds_write_b16_d16_hi v2, v3 offset:64
	v_sub_f32_e32 v3, v38, v0
	v_mul_f32_e32 v3, v3, v1
	v_bfe_u32 v4, v3, 16, 1
	v_add3_u32 v3, v3, v4, s90
	ds_write_b16_d16_hi v2, v3 offset:128
	v_sub_f32_e32 v3, v54, v0
	v_mul_f32_e32 v3, v3, v1
	v_bfe_u32 v4, v3, 16, 1
	v_add3_u32 v3, v3, v4, s90
	ds_write_b16_d16_hi v2, v3 offset:192
	v_sub_f32_e32 v3, v102, v0
	v_mul_f32_e32 v3, v3, v1
	v_bfe_u32 v4, v3, 16, 1
	v_add3_u32 v3, v3, v4, s90
	ds_write_b16_d16_hi v2, v3 offset:256
	v_sub_f32_e32 v3, v118, v0
	v_mul_f32_e32 v3, v3, v1
	v_bfe_u32 v4, v3, 16, 1
	v_add3_u32 v3, v3, v4, s90
	ds_write_b16_d16_hi v2, v3 offset:320
	v_sub_f32_e32 v3, v86, v0
	v_mul_f32_e32 v3, v3, v1
	v_bfe_u32 v4, v3, 16, 1
	v_add3_u32 v3, v3, v4, s90
	v_sub_f32_e32 v0, v70, v0
	ds_write_b16_d16_hi v2, v3 offset:384
	v_mul_f32_e32 v3, v0, v1
	v_pk_add_f32 v[0:1], v[146:147], v[34:35]
	s_nop 0
	v_pk_mul_f32 v[0:1], v[0:1], s[26:27] op_sel_hi:[1,0]
	s_nop 0
	v_fma_f32 v1, -v0, v0, v1
	v_max_f32_e32 v1, 0, v1
	v_add_f32_e32 v1, 0x358637bd, v1
	v_mul_f32_e32 v4, 0x4b800000, v1
	v_cmp_gt_f32_e32 vcc, s89, v1
	s_nop 1
	v_cndmask_b32_e32 v1, v1, v4, vcc
	v_rsq_f32_e32 v1, v1
	v_bfe_u32 v4, v3, 16, 1
	v_add3_u32 v3, v3, v4, s90
	ds_write_b16_d16_hi v2, v3 offset:448
	v_mul_f32_e32 v2, 0x45800000, v1
	v_cndmask_b32_e32 v1, v1, v2, vcc
	v_sub_f32_e32 v3, v23, v0
	v_lshlrev_b32_e32 v2, 10, v212
	v_mul_f32_e32 v3, v3, v1
	v_bfe_u32 v4, v3, 16, 1
	v_add3_u32 v17, 0, v2, v16
	v_sub_f32_e32 v2, v7, v0
	v_add3_u32 v3, v3, v4, s90
	v_mul_f32_e32 v2, v2, v1
	ds_write_b16_d16_hi v17, v3
	v_bfe_u32 v3, v2, 16, 1
	v_add3_u32 v2, v2, v3, s90
	ds_write_b16_d16_hi v17, v2 offset:64
	v_sub_f32_e32 v2, v39, v0
	v_mul_f32_e32 v2, v2, v1
	v_bfe_u32 v3, v2, 16, 1
	v_add3_u32 v2, v2, v3, s90
	ds_write_b16_d16_hi v17, v2 offset:128
	v_sub_f32_e32 v2, v55, v0
	v_mul_f32_e32 v2, v2, v1
	v_bfe_u32 v3, v2, 16, 1
	v_add3_u32 v2, v2, v3, s90
	ds_write_b16_d16_hi v17, v2 offset:192
	v_sub_f32_e32 v2, v103, v0
	v_mul_f32_e32 v2, v2, v1
	v_bfe_u32 v3, v2, 16, 1
	v_add3_u32 v2, v2, v3, s90
	ds_write_b16_d16_hi v17, v2 offset:256
	v_sub_f32_e32 v2, v119, v0
	v_mul_f32_e32 v2, v2, v1
	v_bfe_u32 v3, v2, 16, 1
	v_add3_u32 v2, v2, v3, s90
	ds_write_b16_d16_hi v17, v2 offset:320
	v_sub_f32_e32 v2, v87, v0
	v_sub_f32_e32 v0, v71, v0
	v_mul_f32_e32 v2, v2, v1
	v_mul_f32_e32 v18, v0, v1
	v_lshlrev_b32_e32 v0, 1, v211
	v_bfe_u32 v3, v2, 16, 1
	v_subrev_u32_e32 v0, s6, v0
	v_add3_u32 v2, v2, v3, s90
	v_lshl_add_u32 v0, v0, 2, s4
	ds_write_b16_d16_hi v17, v2 offset:384
	ds_read2_b64 v[0:3], v0 offset0:128 offset1:129
	v_lshlrev_b32_e32 v4, 1, v209
	v_subrev_u32_e32 v4, s6, v4
	v_lshl_add_u32 v4, v4, 2, s4
	ds_read2_b64 v[4:7], v4 offset0:128 offset1:129
	s_waitcnt lgkmcnt(1)
	v_pk_add_f32 v[0:1], v[140:141], v[0:1]
	s_nop 0
	v_pk_mul_f32 v[0:1], v[0:1], s[26:27] op_sel_hi:[1,0]
	s_nop 0
	v_fma_f32 v1, -v0, v0, v1
	v_max_f32_e32 v1, 0, v1
	v_add_f32_e32 v1, 0x358637bd, v1
	v_mul_f32_e32 v19, 0x4b800000, v1
	v_cmp_gt_f32_e32 vcc, s89, v1
	v_sub_f32_e32 v8, v8, v0
	s_nop 0
	v_cndmask_b32_e32 v1, v1, v19, vcc
	v_rsq_f32_e32 v1, v1
	v_bfe_u32 v19, v18, 16, 1
	v_add3_u32 v18, v18, v19, s90
	ds_write_b16_d16_hi v17, v18 offset:448
	v_mul_f32_e32 v17, 0x45800000, v1
	v_cndmask_b32_e32 v1, v1, v17, vcc
	v_sub_f32_e32 v18, v24, v0
	v_mul_f32_e32 v18, v18, v1
	v_lshlrev_b32_e32 v17, 10, v211
	v_bfe_u32 v19, v18, 16, 1
	v_add3_u32 v18, v18, v19, s90
	v_add3_u32 v17, 0, v17, v16
	v_mul_f32_e32 v8, v8, v1
	ds_write_b16_d16_hi v17, v18
	v_bfe_u32 v18, v8, 16, 1
	v_add3_u32 v8, v8, v18, s90
	ds_write_b16_d16_hi v17, v8 offset:64
	v_sub_f32_e32 v8, v40, v0
	v_mul_f32_e32 v8, v8, v1
	v_bfe_u32 v18, v8, 16, 1
	v_add3_u32 v8, v8, v18, s90
	ds_write_b16_d16_hi v17, v8 offset:128
	v_sub_f32_e32 v8, v56, v0
	v_mul_f32_e32 v8, v8, v1
	v_bfe_u32 v18, v8, 16, 1
	v_add3_u32 v8, v8, v18, s90
	ds_write_b16_d16_hi v17, v8 offset:192
	v_sub_f32_e32 v8, v104, v0
	v_mul_f32_e32 v8, v8, v1
	v_bfe_u32 v18, v8, 16, 1
	v_add3_u32 v8, v8, v18, s90
	ds_write_b16_d16_hi v17, v8 offset:256
	v_sub_f32_e32 v8, v120, v0
	v_mul_f32_e32 v8, v8, v1
	v_bfe_u32 v18, v8, 16, 1
	v_add3_u32 v8, v8, v18, s90
	ds_write_b16_d16_hi v17, v8 offset:320
	v_sub_f32_e32 v8, v88, v0
	v_mul_f32_e32 v8, v8, v1
	v_bfe_u32 v18, v8, 16, 1
	v_add3_u32 v8, v8, v18, s90
	v_sub_f32_e32 v0, v72, v0
	ds_write_b16_d16_hi v17, v8 offset:384
	v_mul_f32_e32 v8, v0, v1
	v_pk_add_f32 v[0:1], v[142:143], v[2:3]
	s_nop 0
	v_pk_mul_f32 v[0:1], v[0:1], s[26:27] op_sel_hi:[1,0]
	s_nop 0
	v_fma_f32 v1, -v0, v0, v1
	v_max_f32_e32 v1, 0, v1
	v_add_f32_e32 v1, 0x358637bd, v1
	v_mul_f32_e32 v2, 0x4b800000, v1
	v_cmp_gt_f32_e32 vcc, s89, v1
	v_sub_f32_e32 v3, v25, v0
	s_nop 0
	v_cndmask_b32_e32 v1, v1, v2, vcc
	v_rsq_f32_e32 v1, v1
	v_bfe_u32 v2, v8, 16, 1
	v_add3_u32 v2, v8, v2, s90
	ds_write_b16_d16_hi v17, v2 offset:448
	v_mul_f32_e32 v2, 0x45800000, v1
	v_cndmask_b32_e32 v1, v1, v2, vcc
	v_mul_f32_e32 v3, v3, v1
	v_lshlrev_b32_e32 v2, 10, v210
	v_bfe_u32 v8, v3, 16, 1
	v_add3_u32 v3, v3, v8, s90
	v_add3_u32 v2, 0, v2, v16
	ds_write_b16_d16_hi v2, v3
	v_sub_f32_e32 v3, v9, v0
	v_mul_f32_e32 v3, v3, v1
	v_bfe_u32 v8, v3, 16, 1
	v_add3_u32 v3, v3, v8, s90
	ds_write_b16_d16_hi v2, v3 offset:64
	v_sub_f32_e32 v3, v41, v0
	v_mul_f32_e32 v3, v3, v1
	v_bfe_u32 v8, v3, 16, 1
	v_add3_u32 v3, v3, v8, s90
	ds_write_b16_d16_hi v2, v3 offset:128
	v_sub_f32_e32 v3, v57, v0
	v_mul_f32_e32 v3, v3, v1
	v_bfe_u32 v8, v3, 16, 1
	v_add3_u32 v3, v3, v8, s90
	ds_write_b16_d16_hi v2, v3 offset:192
	v_sub_f32_e32 v3, v105, v0
	v_mul_f32_e32 v3, v3, v1
	v_bfe_u32 v8, v3, 16, 1
	v_add3_u32 v3, v3, v8, s90
	ds_write_b16_d16_hi v2, v3 offset:256
	v_sub_f32_e32 v3, v121, v0
	v_mul_f32_e32 v3, v3, v1
	v_bfe_u32 v8, v3, 16, 1
	v_add3_u32 v3, v3, v8, s90
	ds_write_b16_d16_hi v2, v3 offset:320
	v_sub_f32_e32 v3, v89, v0
	v_mul_f32_e32 v3, v3, v1
	v_bfe_u32 v8, v3, 16, 1
	v_add3_u32 v3, v3, v8, s90
	v_sub_f32_e32 v0, v73, v0
	ds_write_b16_d16_hi v2, v3 offset:384
	v_mul_f32_e32 v3, v0, v1
	s_waitcnt lgkmcnt(14)
; #define LAS __attribute__((address_space(3)))
; __device__ __forceinline__ bf16_t f2bf(float f) { unsigned u = __builtin_bit_cast(unsigned, f); return (bf16_t)((u + 0x7fffu + ((u >> 16) & 1u)) >> 16); }
; __device__ __forceinline__ int crow(int r, int hi) { return (r & 3) + 8 * (r >> 2) + 4 * hi; }
; __device__ __forceinline__ int crow(int r, int hi) { return (r & 3) + 8 * (r >> 2) + 4 * hi; }
; template <int DK, int DV, bool MLSTM>
; __device__ __forceinline__ void out_unit2(LAS unsigned char* lds, LAS unsigned char* ldstab, const OutArgs a, const int wv) {
;     ...
;     for (int r = 0; r < 16; ++r) {
;         const int row = 32 * rb + crow(r, hi);
;         const float t1 = s1[r] + exch[((1 - dh) * 128 + row) * 2], t2 = s2[r] + exch[((1 - dh) * 128 + row) * 2 + 1];
;         float mean, inv;
;         if (MLSTM) { mean = 0.f; inv = rsqrtf(t2 * (1.f / DV) + EPS); }
;         else { mean = t1 * (1.f / DV); inv = rsqrtf(fmaxf(t2 * (1.f / DV) - mean * mean, 0.f) + EPS); }
; #pragma unroll
;         for (int nb = 0; nb < NB; ++nb) { const int col = dh * (DV / 2) + 32 * nb + r32;
;             *(LAS bf16_t*)(lds + row * TP + col * 2) = f2bf((o[nb][r] - mean) * inv); }
	v_pk_add_f32 v[0:1], v[136:137], v[4:5]
	s_nop 0
	v_pk_mul_f32 v[0:1], v[0:1], s[26:27] op_sel_hi:[1,0]
	s_nop 0
	v_fma_f32 v1, -v0, v0, v1
	v_max_f32_e32 v1, 0, v1
	v_add_f32_e32 v1, 0x358637bd, v1
	v_mul_f32_e32 v4, 0x4b800000, v1
	v_cmp_gt_f32_e32 vcc, s89, v1
	s_nop 1
	v_cndmask_b32_e32 v1, v1, v4, vcc
	v_rsq_f32_e32 v1, v1
	v_bfe_u32 v4, v3, 16, 1
	v_add3_u32 v3, v3, v4, s90
	ds_write_b16_d16_hi v2, v3 offset:448
	v_mul_f32_e32 v2, 0x45800000, v1
	v_cndmask_b32_e32 v1, v1, v2, vcc
	v_sub_f32_e32 v3, v26, v0
	v_mul_f32_e32 v3, v3, v1
	v_lshlrev_b32_e32 v2, 10, v209
	v_bfe_u32 v4, v3, 16, 1
	v_add3_u32 v3, v3, v4, s90
	v_add3_u32 v2, 0, v2, v16
	ds_write_b16_d16_hi v2, v3
	v_sub_f32_e32 v3, v10, v0
	v_mul_f32_e32 v3, v3, v1
	v_bfe_u32 v4, v3, 16, 1
	v_add3_u32 v3, v3, v4, s90
	ds_write_b16_d16_hi v2, v3 offset:64
	v_sub_f32_e32 v3, v42, v0
	v_mul_f32_e32 v3, v3, v1
	v_bfe_u32 v4, v3, 16, 1
	v_add3_u32 v3, v3, v4, s90
	ds_write_b16_d16_hi v2, v3 offset:128
	v_sub_f32_e32 v3, v58, v0
	v_mul_f32_e32 v3, v3, v1
	v_bfe_u32 v4, v3, 16, 1
	v_add3_u32 v3, v3, v4, s90
	ds_write_b16_d16_hi v2, v3 offset:192
	v_sub_f32_e32 v3, v106, v0
	v_mul_f32_e32 v3, v3, v1
	v_bfe_u32 v4, v3, 16, 1
	v_add3_u32 v3, v3, v4, s90
	ds_write_b16_d16_hi v2, v3 offset:256
	v_sub_f32_e32 v3, v122, v0
	v_mul_f32_e32 v3, v3, v1
	v_bfe_u32 v4, v3, 16, 1
	v_add3_u32 v3, v3, v4, s90
	ds_write_b16_d16_hi v2, v3 offset:320
	v_sub_f32_e32 v3, v90, v0
	v_mul_f32_e32 v3, v3, v1
	v_bfe_u32 v4, v3, 16, 1
	v_add3_u32 v3, v3, v4, s90
	v_sub_f32_e32 v0, v74, v0
	ds_write_b16_d16_hi v2, v3 offset:384
	v_mul_f32_e32 v3, v0, v1
	v_pk_add_f32 v[0:1], v[138:139], v[6:7]
	s_nop 0
	v_pk_mul_f32 v[0:1], v[0:1], s[26:27] op_sel_hi:[1,0]
	s_nop 0
	v_fma_f32 v1, -v0, v0, v1
	v_max_f32_e32 v1, 0, v1
	v_add_f32_e32 v1, 0x358637bd, v1
	v_mul_f32_e32 v4, 0x4b800000, v1
	v_cmp_gt_f32_e32 vcc, s89, v1
	s_nop 1
	v_cndmask_b32_e32 v1, v1, v4, vcc
	v_rsq_f32_e32 v1, v1
	v_bfe_u32 v4, v3, 16, 1
	v_add3_u32 v3, v3, v4, s90
	ds_write_b16_d16_hi v2, v3 offset:448
	v_mul_f32_e32 v2, 0x45800000, v1
	v_cndmask_b32_e32 v1, v1, v2, vcc
	v_sub_f32_e32 v3, v27, v0
	v_lshlrev_b32_e32 v2, 10, v208
	v_mul_f32_e32 v3, v3, v1
	v_bfe_u32 v4, v3, 16, 1
	v_add3_u32 v8, 0, v2, v16
	v_sub_f32_e32 v2, v11, v0
	v_add3_u32 v3, v3, v4, s90
	v_mul_f32_e32 v2, v2, v1
	ds_write_b16_d16_hi v8, v3
	v_bfe_u32 v3, v2, 16, 1
	v_add3_u32 v2, v2, v3, s90
	ds_write_b16_d16_hi v8, v2 offset:64
	v_sub_f32_e32 v2, v43, v0
	v_mul_f32_e32 v2, v2, v1
	v_bfe_u32 v3, v2, 16, 1
	v_add3_u32 v2, v2, v3, s90
	ds_write_b16_d16_hi v8, v2 offset:128
	v_sub_f32_e32 v2, v59, v0
	v_mul_f32_e32 v2, v2, v1
	v_bfe_u32 v3, v2, 16, 1
	v_add3_u32 v2, v2, v3, s90
	ds_write_b16_d16_hi v8, v2 offset:192
	v_sub_f32_e32 v2, v107, v0
	v_mul_f32_e32 v2, v2, v1
	v_bfe_u32 v3, v2, 16, 1
	v_add3_u32 v2, v2, v3, s90
	ds_write_b16_d16_hi v8, v2 offset:256
	v_sub_f32_e32 v2, v123, v0
	v_mul_f32_e32 v2, v2, v1
	v_bfe_u32 v3, v2, 16, 1
	v_add3_u32 v2, v2, v3, s90
	ds_write_b16_d16_hi v8, v2 offset:320
	v_sub_f32_e32 v2, v91, v0
	v_sub_f32_e32 v0, v75, v0
	v_mul_f32_e32 v2, v2, v1
	v_mul_f32_e32 v9, v0, v1
	v_lshlrev_b32_e32 v0, 1, v207
	v_bfe_u32 v3, v2, 16, 1
	v_subrev_u32_e32 v0, s6, v0
	v_add3_u32 v2, v2, v3, s90
	v_lshl_add_u32 v0, v0, 2, s4
	ds_write_b16_d16_hi v8, v2 offset:384
	ds_read2_b64 v[0:3], v0 offset0:128 offset1:129
	v_lshlrev_b32_e32 v4, 1, v162
	v_subrev_u32_e32 v4, s6, v4
	v_lshl_add_u32 v4, v4, 2, s4
	ds_read2_b64 v[4:7], v4 offset0:128 offset1:129
	s_waitcnt lgkmcnt(1)
	v_pk_add_f32 v[0:1], v[132:133], v[0:1]
	s_nop 0
	v_pk_mul_f32 v[0:1], v[0:1], s[26:27] op_sel_hi:[1,0]
	s_nop 0
	v_fma_f32 v1, -v0, v0, v1
	v_max_f32_e32 v1, 0, v1
	v_add_f32_e32 v1, 0x358637bd, v1
	v_mul_f32_e32 v10, 0x4b800000, v1
	v_cmp_gt_f32_e32 vcc, s89, v1
	s_nop 1
	v_cndmask_b32_e32 v1, v1, v10, vcc
	v_rsq_f32_e32 v1, v1
	v_bfe_u32 v10, v9, 16, 1
	v_add3_u32 v9, v9, v10, s90
	ds_write_b16_d16_hi v8, v9 offset:448
	v_mul_f32_e32 v8, 0x45800000, v1
	v_cndmask_b32_e32 v1, v1, v8, vcc
	v_sub_f32_e32 v9, v28, v0
	v_mul_f32_e32 v9, v9, v1
	v_lshlrev_b32_e32 v8, 10, v207
	v_bfe_u32 v10, v9, 16, 1
	v_add3_u32 v9, v9, v10, s90
	v_add3_u32 v8, 0, v8, v16
	ds_write_b16_d16_hi v8, v9
	v_sub_f32_e32 v9, v12, v0
	v_mul_f32_e32 v9, v9, v1
	v_bfe_u32 v10, v9, 16, 1
	v_add3_u32 v9, v9, v10, s90
	ds_write_b16_d16_hi v8, v9 offset:64
	v_sub_f32_e32 v9, v44, v0
	v_mul_f32_e32 v9, v9, v1
	v_bfe_u32 v10, v9, 16, 1
	v_add3_u32 v9, v9, v10, s90
	ds_write_b16_d16_hi v8, v9 offset:128
	v_sub_f32_e32 v9, v60, v0
	v_mul_f32_e32 v9, v9, v1
	v_bfe_u32 v10, v9, 16, 1
	v_add3_u32 v9, v9, v10, s90
	ds_write_b16_d16_hi v8, v9 offset:192
	v_sub_f32_e32 v9, v108, v0
	v_mul_f32_e32 v9, v9, v1
	v_bfe_u32 v10, v9, 16, 1
	v_add3_u32 v9, v9, v10, s90
	ds_write_b16_d16_hi v8, v9 offset:256
	v_sub_f32_e32 v9, v124, v0
	v_mul_f32_e32 v9, v9, v1
	v_bfe_u32 v10, v9, 16, 1
	v_add3_u32 v9, v9, v10, s90
	ds_write_b16_d16_hi v8, v9 offset:320
	v_sub_f32_e32 v9, v92, v0
	v_mul_f32_e32 v9, v9, v1
	v_bfe_u32 v10, v9, 16, 1
	v_add3_u32 v9, v9, v10, s90
	v_sub_f32_e32 v0, v76, v0
	ds_write_b16_d16_hi v8, v9 offset:384
	v_mul_f32_e32 v9, v0, v1
	v_pk_add_f32 v[0:1], v[134:135], v[2:3]
	s_nop 0
	v_pk_mul_f32 v[0:1], v[0:1], s[26:27] op_sel_hi:[1,0]
	s_nop 0
	v_fma_f32 v1, -v0, v0, v1
	v_max_f32_e32 v1, 0, v1
	v_add_f32_e32 v1, 0x358637bd, v1
	v_mul_f32_e32 v2, 0x4b800000, v1
	v_cmp_gt_f32_e32 vcc, s89, v1
	v_sub_f32_e32 v3, v29, v0
	s_nop 0
	v_cndmask_b32_e32 v1, v1, v2, vcc
	v_rsq_f32_e32 v1, v1
	v_bfe_u32 v2, v9, 16, 1
	v_add3_u32 v2, v9, v2, s90
	ds_write_b16_d16_hi v8, v2 offset:448
	v_mul_f32_e32 v2, 0x45800000, v1
	v_cndmask_b32_e32 v1, v1, v2, vcc
	v_mul_f32_e32 v3, v3, v1
	v_lshlrev_b32_e32 v2, 10, v206
	v_bfe_u32 v8, v3, 16, 1
	v_add3_u32 v3, v3, v8, s90
	v_add3_u32 v2, 0, v2, v16
	ds_write_b16_d16_hi v2, v3
	v_sub_f32_e32 v3, v13, v0
	v_mul_f32_e32 v3, v3, v1
	v_bfe_u32 v8, v3, 16, 1
	v_add3_u32 v3, v3, v8, s90
	ds_write_b16_d16_hi v2, v3 offset:64
	v_sub_f32_e32 v3, v45, v0
	v_mul_f32_e32 v3, v3, v1
	v_bfe_u32 v8, v3, 16, 1
	v_add3_u32 v3, v3, v8, s90
	ds_write_b16_d16_hi v2, v3 offset:128
	v_sub_f32_e32 v3, v61, v0
	v_mul_f32_e32 v3, v3, v1
	v_bfe_u32 v8, v3, 16, 1
	v_add3_u32 v3, v3, v8, s90
	ds_write_b16_d16_hi v2, v3 offset:192
	v_sub_f32_e32 v3, v109, v0
	v_mul_f32_e32 v3, v3, v1
	v_bfe_u32 v8, v3, 16, 1
	v_add3_u32 v3, v3, v8, s90
	ds_write_b16_d16_hi v2, v3 offset:256
	v_sub_f32_e32 v3, v125, v0
	v_mul_f32_e32 v3, v3, v1
	v_bfe_u32 v8, v3, 16, 1
	v_add3_u32 v3, v3, v8, s90
	ds_write_b16_d16_hi v2, v3 offset:320
	v_sub_f32_e32 v3, v93, v0
	v_mul_f32_e32 v3, v3, v1
	v_bfe_u32 v8, v3, 16, 1
	v_add3_u32 v3, v3, v8, s90
	v_sub_f32_e32 v0, v77, v0
	ds_write_b16_d16_hi v2, v3 offset:384
	v_mul_f32_e32 v3, v0, v1
	s_waitcnt lgkmcnt(14)
; #define LAS __attribute__((address_space(3)))
; template <int DK, int DV, bool MLSTM>
; __device__ __forceinline__ void out_unit2(LAS unsigned char* lds, LAS unsigned char* ldstab, const OutArgs a, const int wv) {
;     ...
;     for (int r = 0; r < 16; ++r) {
;         const int row = 32 * rb + crow(r, hi);
;         const float t1 = s1[r] + exch[((1 - dh) * 128 + row) * 2], t2 = s2[r] + exch[((1 - dh) * 128 + row) * 2 + 1];
;         float mean, inv;
;         if (MLSTM) { mean = 0.f; inv = rsqrtf(t2 * (1.f / DV) + EPS); }
;         else { mean = t1 * (1.f / DV); inv = rsqrtf(fmaxf(t2 * (1.f / DV) - mean * mean, 0.f) + EPS); }
; #pragma unroll
;         for (int nb = 0; nb < NB; ++nb) { const int col = dh * (DV / 2) + 32 * nb + r32;
;             *(LAS bf16_t*)(lds + row * TP + col * 2) = f2bf((o[nb][r] - mean) * inv); }
;     }
;     __syncthreads();
;     constexpr int CPR = DV / 8;
; #pragma unroll 1
;     for (int id = tid; id < 128 * CPR; id += 512) { const int row = id / CPR, ch = id % CPR;
;         const u32x4 y = *(const LAS u32x4*)(lds + row * TP + ch * 16);
;         const f32x4 g0 = *(const f32x4*)(a.gain + 8 * ch), g1 = *(const f32x4*)(a.gain + 8 * ch + 4);
;         float yv[8] = {bf_lo(y.x), bf_hi(y.x), bf_lo(y.y), bf_hi(y.y), bf_lo(y.z), bf_hi(y.z), bf_lo(y.w), bf_hi(y.w)};
;         float gv[8];
;         if (MLSTM) { const u32x4 g = *(const u32x4*)(a.G + (size_t)row * a.ldg + 8 * ch);
;             gv[0] = bf_lo(g.x); gv[1] = bf_hi(g.x); gv[2] = bf_lo(g.y); gv[3] = bf_hi(g.y); gv[4] = bf_lo(g.z); gv[5] = bf_hi(g.z); gv[6] = bf_lo(g.w); gv[7] = bf_hi(g.w); }
;         else { const u32x2 g = *(const u32x2*)(a.G8 + (size_t)row * a.ldg8 + 8 * ch);
;             const f32x2 e0 = __builtin_amdgcn_cvt_pk_f32_fp8((int)g.x, false), e1 = __builtin_amdgcn_cvt_pk_f32_fp8((int)g.x, true), e2 = __builtin_amdgcn_cvt_pk_f32_fp8((int)g.y, false), e3 = __builtin_amdgcn_cvt_pk_f32_fp8((int)g.y, true);
;             gv[0] = e0[0] * a.g8inv; gv[1] = e0[1] * a.g8inv; gv[2] = e1[0] * a.g8inv; gv[3] = e1[1] * a.g8inv; gv[4] = e2[0] * a.g8inv; gv[5] = e2[1] * a.g8inv; gv[6] = e3[0] * a.g8inv; gv[7] = e3[1] * a.g8inv; }
;         float gn[8] = {g0[0], g0[1], g0[2], g0[3], g1[0], g1[1], g1[2], g1[3]};
;         float ov[8];
; #pragma unroll
;         for (int i = 0; i < 8; ++i) ov[i] = yv[i] * gn[i] * (MLSTM ? sigmoidf_(gv[i]) : siluf_(gv[i]));
	v_pk_add_f32 v[0:1], v[128:129], v[4:5]
	s_nop 0
	v_pk_mul_f32 v[0:1], v[0:1], s[26:27] op_sel_hi:[1,0]
	s_nop 0
	v_fma_f32 v1, -v0, v0, v1
	v_max_f32_e32 v1, 0, v1
	v_add_f32_e32 v1, 0x358637bd, v1
	v_mul_f32_e32 v4, 0x4b800000, v1
	v_cmp_gt_f32_e32 vcc, s89, v1
	s_nop 1
	v_cndmask_b32_e32 v1, v1, v4, vcc
	v_rsq_f32_e32 v1, v1
	v_bfe_u32 v4, v3, 16, 1
	v_add3_u32 v3, v3, v4, s90
	ds_write_b16_d16_hi v2, v3 offset:448
	v_mul_f32_e32 v2, 0x45800000, v1
	v_cndmask_b32_e32 v1, v1, v2, vcc
	v_sub_f32_e32 v3, v30, v0
	v_mul_f32_e32 v3, v3, v1
	v_lshlrev_b32_e32 v2, 10, v162
	v_bfe_u32 v4, v3, 16, 1
	v_add3_u32 v3, v3, v4, s90
	v_add3_u32 v2, 0, v2, v16
	ds_write_b16_d16_hi v2, v3
	v_sub_f32_e32 v3, v14, v0
	v_mul_f32_e32 v3, v3, v1
	v_bfe_u32 v4, v3, 16, 1
	v_add3_u32 v3, v3, v4, s90
	ds_write_b16_d16_hi v2, v3 offset:64
	v_sub_f32_e32 v3, v46, v0
	v_mul_f32_e32 v3, v3, v1
	v_bfe_u32 v4, v3, 16, 1
	v_add3_u32 v3, v3, v4, s90
	ds_write_b16_d16_hi v2, v3 offset:128
	v_sub_f32_e32 v3, v62, v0
	v_mul_f32_e32 v3, v3, v1
	v_bfe_u32 v4, v3, 16, 1
	v_add3_u32 v3, v3, v4, s90
	ds_write_b16_d16_hi v2, v3 offset:192
	v_sub_f32_e32 v3, v110, v0
	v_mul_f32_e32 v3, v3, v1
	v_bfe_u32 v4, v3, 16, 1
	v_add3_u32 v3, v3, v4, s90
	ds_write_b16_d16_hi v2, v3 offset:256
	v_sub_f32_e32 v3, v126, v0
	v_mul_f32_e32 v3, v3, v1
	v_bfe_u32 v4, v3, 16, 1
	v_add3_u32 v3, v3, v4, s90
	ds_write_b16_d16_hi v2, v3 offset:320
	v_sub_f32_e32 v3, v94, v0
	v_mul_f32_e32 v3, v3, v1
	v_bfe_u32 v4, v3, 16, 1
	v_add3_u32 v3, v3, v4, s90
	v_sub_f32_e32 v0, v78, v0
	ds_write_b16_d16_hi v2, v3 offset:384
	v_mul_f32_e32 v3, v0, v1
	v_pk_add_f32 v[0:1], v[130:131], v[6:7]
	s_nop 0
	v_pk_mul_f32 v[0:1], v[0:1], s[26:27] op_sel_hi:[1,0]
	s_nop 0
	v_fma_f32 v1, -v0, v0, v1
	v_max_f32_e32 v1, 0, v1
	v_add_f32_e32 v1, 0x358637bd, v1
	v_mul_f32_e32 v4, 0x4b800000, v1
	v_cmp_gt_f32_e32 vcc, s89, v1
	s_nop 1
	v_cndmask_b32_e32 v1, v1, v4, vcc
	v_rsq_f32_e32 v1, v1
	v_bfe_u32 v4, v3, 16, 1
	v_add3_u32 v3, v3, v4, s90
	ds_write_b16_d16_hi v2, v3 offset:448
	v_mul_f32_e32 v2, 0x45800000, v1
	v_cndmask_b32_e32 v1, v1, v2, vcc
	v_sub_f32_e32 v3, v31, v0
	v_mul_f32_e32 v3, v3, v1
	v_lshlrev_b32_e32 v2, 10, v160
	v_bfe_u32 v4, v3, 16, 1
	v_add3_u32 v3, v3, v4, s90
	v_add3_u32 v2, 0, v2, v16
	ds_write_b16_d16_hi v2, v3
	v_sub_f32_e32 v3, v15, v0
	v_mul_f32_e32 v3, v3, v1
	v_bfe_u32 v4, v3, 16, 1
	v_add3_u32 v3, v3, v4, s90
	ds_write_b16_d16_hi v2, v3 offset:64
	v_sub_f32_e32 v3, v47, v0
	v_mul_f32_e32 v3, v3, v1
	v_bfe_u32 v4, v3, 16, 1
	v_add3_u32 v3, v3, v4, s90
	ds_write_b16_d16_hi v2, v3 offset:128
	v_sub_f32_e32 v3, v63, v0
	v_mul_f32_e32 v3, v3, v1
	v_bfe_u32 v4, v3, 16, 1
	v_add3_u32 v3, v3, v4, s90
	ds_write_b16_d16_hi v2, v3 offset:192
	v_sub_f32_e32 v3, v111, v0
	v_mul_f32_e32 v3, v3, v1
	v_bfe_u32 v4, v3, 16, 1
	v_add3_u32 v3, v3, v4, s90
	ds_write_b16_d16_hi v2, v3 offset:256
	v_sub_f32_e32 v3, v127, v0
	v_mul_f32_e32 v3, v3, v1
	v_bfe_u32 v4, v3, 16, 1
	v_add3_u32 v3, v3, v4, s90
	ds_write_b16_d16_hi v2, v3 offset:320
	v_sub_f32_e32 v3, v95, v0
	v_sub_f32_e32 v0, v79, v0
	v_mul_f32_e32 v3, v3, v1
	v_mul_f32_e32 v0, v0, v1
	v_bfe_u32 v4, v3, 16, 1
	v_bfe_u32 v1, v0, 16, 1
	v_add3_u32 v3, v3, v4, s90
	v_add3_u32 v0, v0, v1, s90
	v_cmp_gt_i32_e32 vcc, s88, v232
	ds_write_b16_d16_hi v2, v3 offset:384
	ds_write_b16_d16_hi v2, v0 offset:448
	s_waitcnt lgkmcnt(0)
	s_barrier
	s_and_saveexec_b64 s[36:37], vcc
	s_cbranch_execz .LBB0_4301
	s_lshl_b32 s4, s8, 2
	s_add_u32 s38, s51, s4
	s_addc_u32 s39, s52, 0
	s_lshl_b64 s[2:3], s[2:3], 11
	s_add_u32 s4, s53, s2
	s_addc_u32 s5, s54, s3
	s_add_u32 s40, s4, s8
	s_addc_u32 s41, s5, 0
	s_add_u32 s2, s55, s2
	s_addc_u32 s3, s56, s3
	s_add_u32 s42, s2, s8
	s_addc_u32 s43, s3, 0
	v_lshl_add_u32 v4, v232, 4, 0
	v_lshlrev_b32_e32 v5, 3, v232
	s_mov_b64 s[44:45], 0
	v_and_b32_e32 v6, 63, v232
	v_lshrrev_b32_e32 v7, 6, v232
	v_lshlrev_b32_e32 v8, 5, v6
	v_lshlrev_b32_e32 v5, 3, v6
	v_lshl_add_u32 v5, v7, 11, v5
	ds_read_b128 v[0:3], v4
	v_add_u32_e32 v4, 0x2000, v4
	global_load_dwordx4 v[40:43], v8, s[38:39]
	global_load_dwordx4 v[44:47], v8, s[38:39] offset:16
	global_load_dwordx2 v[30:31], v5, s[40:41]
	v_add_u32_e32 v22, 0x4000, v5
	s_nop 0
	global_load_dwordx2 v[6:7], v22, s[40:41]
	v_add_u32_e32 v22, 0x4000, v22
	v_mov_b32_e32 v162, v163
	s_movk_i32 s44, 8
	s_waitcnt vmcnt(1)
.Ldloop1:
	s_waitcnt vmcnt(2) lgkmcnt(0)
	v_lshlrev_b32_e32 v10, 16, v0
	v_and_b32_e32 v11, 0xffff0000, v0
	v_lshlrev_b32_e32 v12, 16, v1
	v_and_b32_e32 v13, 0xffff0000, v1
	v_lshlrev_b32_e32 v14, 16, v2
	v_and_b32_e32 v15, 0xffff0000, v2
	v_lshlrev_b32_e32 v16, 16, v3
	v_and_b32_e32 v17, 0xffff0000, v3
	v_cvt_pk_f32_fp8_e32 v[32:33], v30
	v_cvt_pk_f32_fp8_sdwa v[34:35], v30 src0_sel:WORD_1
	v_cvt_pk_f32_fp8_e32 v[36:37], v31
	v_cvt_pk_f32_fp8_sdwa v[38:39], v31 src0_sel:WORD_1
	ds_read_b128 v[0:3], v4
	v_add_u32_e32 v4, 0x2000, v4
	s_cmp_eq_u32 s44, 1
	s_cbranch_scc1 .Ldloop1a
	global_load_dwordx2 v[30:31], v22, s[40:41]
	v_add_u32_e32 v22, 0x4000, v22
; #define LAS __attribute__((address_space(3)))
; __device__ __forceinline__ float sigmoidf_(float x) { return 1.f / (1.f + __expf(-x)); }
; __device__ __forceinline__ float siluf_(float x) { return x / (1.f + __expf(-x)); }
; template <int DK, int DV, bool MLSTM>
; __device__ __forceinline__ void out_unit2(LAS unsigned char* lds, LAS unsigned char* ldstab, const OutArgs a, const int wv) {
;     ...
; #pragma unroll 1
;     for (int id = tid; id < 128 * CPR; id += 512) { const int row = id / CPR, ch = id % CPR;
;         const u32x4 y = *(const LAS u32x4*)(lds + row * TP + ch * 16);
;         const f32x4 g0 = *(const f32x4*)(a.gain + 8 * ch), g1 = *(const f32x4*)(a.gain + 8 * ch + 4);
;         float yv[8] = {bf_lo(y.x), bf_hi(y.x), bf_lo(y.y), bf_hi(y.y), bf_lo(y.z), bf_hi(y.z), bf_lo(y.w), bf_hi(y.w)};
;         float gv[8];
;         if (MLSTM) { const u32x4 g = *(const u32x4*)(a.G + (size_t)row * a.ldg + 8 * ch);
;             gv[0] = bf_lo(g.x); gv[1] = bf_hi(g.x); gv[2] = bf_lo(g.y); gv[3] = bf_hi(g.y); gv[4] = bf_lo(g.z); gv[5] = bf_hi(g.z); gv[6] = bf_lo(g.w); gv[7] = bf_hi(g.w); }
;         else { const u32x2 g = *(const u32x2*)(a.G8 + (size_t)row * a.ldg8 + 8 * ch);
;             const f32x2 e0 = __builtin_amdgcn_cvt_pk_f32_fp8((int)g.x, false), e1 = __builtin_amdgcn_cvt_pk_f32_fp8((int)g.x, true), e2 = __builtin_amdgcn_cvt_pk_f32_fp8((int)g.y, false), e3 = __builtin_amdgcn_cvt_pk_f32_fp8((int)g.y, true);
;             gv[0] = e0[0] * a.g8inv; gv[1] = e0[1] * a.g8inv; gv[2] = e1[0] * a.g8inv; gv[3] = e1[1] * a.g8inv; gv[4] = e2[0] * a.g8inv; gv[5] = e2[1] * a.g8inv; gv[6] = e3[0] * a.g8inv; gv[7] = e3[1] * a.g8inv; }
;         float gn[8] = {g0[0], g0[1], g0[2], g0[3], g1[0], g1[1], g1[2], g1[3]};
;         float ov[8];
; #pragma unroll
;         for (int i = 0; i < 8; ++i) ov[i] = yv[i] * gn[i] * (MLSTM ? sigmoidf_(gv[i]) : siluf_(gv[i]));
;         u32x2 w; w.x = pg8::pk4_fp8c(ov[0] * a.oscale, ov[1] * a.oscale, ov[2] * a.oscale, ov[3] * a.oscale); w.y = pg8::pk4_fp8c(ov[4] * a.oscale, ov[5] * a.oscale, ov[6] * a.oscale, ov[7] * a.oscale);
;         *(u32x2*)(a.Out + (size_t)row * a.ldo + 8 * ch) = w; }
.Ldloop1a:
	v_pk_mul_f32 v[10:11], v[40:41], v[10:11]
	v_pk_mul_f32 v[12:13], v[42:43], v[12:13]
	v_pk_mul_f32 v[14:15], v[44:45], v[14:15]
	v_pk_mul_f32 v[16:17], v[46:47], v[16:17]
	v_pk_mul_f32 v[32:33], v[32:33], v[162:163]
	v_pk_mul_f32 v[34:35], v[34:35], v[162:163]
	v_pk_mul_f32 v[36:37], v[36:37], v[162:163]
	v_pk_mul_f32 v[38:39], v[38:39], v[162:163]
	v_mul_f32_e32 v48, 0xbfb8aa3b, v32
	v_mul_f32_e32 v49, 0xbfb8aa3b, v33
	v_mul_f32_e32 v50, 0xbfb8aa3b, v34
	v_mul_f32_e32 v51, 0xbfb8aa3b, v35
	v_mul_f32_e32 v52, 0xbfb8aa3b, v36
	v_mul_f32_e32 v53, 0xbfb8aa3b, v37
	v_mul_f32_e32 v54, 0xbfb8aa3b, v38
	v_mul_f32_e32 v55, 0xbfb8aa3b, v39
	v_exp_f32_e32 v48, v48
	v_exp_f32_e32 v49, v49
	v_exp_f32_e32 v50, v50
	v_exp_f32_e32 v51, v51
	v_exp_f32_e32 v52, v52
	v_exp_f32_e32 v53, v53
	v_exp_f32_e32 v54, v54
	v_exp_f32_e32 v55, v55
	v_add_f32_e32 v48, 1.0, v48
	v_add_f32_e32 v49, 1.0, v49
	v_add_f32_e32 v50, 1.0, v50
	v_add_f32_e32 v51, 1.0, v51
	v_add_f32_e32 v52, 1.0, v52
	v_add_f32_e32 v53, 1.0, v53
	v_add_f32_e32 v54, 1.0, v54
	v_add_f32_e32 v55, 1.0, v55
	v_rcp_f32_e32 v56, v48
	v_rcp_f32_e32 v57, v49
	v_rcp_f32_e32 v58, v50
	v_rcp_f32_e32 v59, v51
	v_rcp_f32_e32 v60, v52
	v_rcp_f32_e32 v61, v53
	v_rcp_f32_e32 v62, v54
	v_rcp_f32_e32 v63, v55
	v_fma_f32 v8, -v48, v56, 1.0
	v_fma_f32 v9, -v49, v57, 1.0
	v_fma_f32 v18, -v50, v58, 1.0
	v_fma_f32 v19, -v51, v59, 1.0
	v_fma_f32 v20, -v52, v60, 1.0
	v_fma_f32 v21, -v53, v61, 1.0
	v_fma_f32 v23, -v54, v62, 1.0
	v_fma_f32 v26, -v55, v63, 1.0
	v_fmac_f32_e32 v56, v8, v56
	v_fmac_f32_e32 v57, v9, v57
	v_fmac_f32_e32 v58, v18, v58
	v_fmac_f32_e32 v59, v19, v59
	v_fmac_f32_e32 v60, v20, v60
	v_fmac_f32_e32 v61, v21, v61
	v_fmac_f32_e32 v62, v23, v62
	v_fmac_f32_e32 v63, v26, v63
	v_mul_f32_e32 v64, v32, v56
	v_mul_f32_e32 v65, v33, v57
	v_mul_f32_e32 v66, v34, v58
	v_mul_f32_e32 v67, v35, v59
	v_mul_f32_e32 v68, v36, v60
	v_mul_f32_e32 v69, v37, v61
	v_mul_f32_e32 v70, v38, v62
	v_mul_f32_e32 v71, v39, v63
	v_fma_f32 v8, -v48, v64, v32
	v_fma_f32 v9, -v49, v65, v33
	v_fma_f32 v18, -v50, v66, v34
	v_fma_f32 v19, -v51, v67, v35
	v_fma_f32 v20, -v52, v68, v36
	v_fma_f32 v21, -v53, v69, v37
	v_fma_f32 v23, -v54, v70, v38
	v_fma_f32 v26, -v55, v71, v39
	v_fmac_f32_e32 v64, v8, v56
	v_fmac_f32_e32 v65, v9, v57
	v_fmac_f32_e32 v66, v18, v58
	v_fmac_f32_e32 v67, v19, v59
	v_fmac_f32_e32 v68, v20, v60
	v_fmac_f32_e32 v69, v21, v61
	v_fmac_f32_e32 v70, v23, v62
	v_fmac_f32_e32 v71, v26, v63
	v_fma_f32 v8, -v48, v64, v32
	v_fma_f32 v9, -v49, v65, v33
	v_fma_f32 v18, -v50, v66, v34
	v_fma_f32 v19, -v51, v67, v35
	v_fma_f32 v20, -v52, v68, v36
	v_fma_f32 v21, -v53, v69, v37
	v_fma_f32 v23, -v54, v70, v38
	v_fma_f32 v26, -v55, v71, v39
	v_fma_f32 v8, v8, v56, v64
	v_fma_f32 v9, v9, v57, v65
	v_fma_f32 v18, v18, v58, v66
	v_fma_f32 v19, v19, v59, v67
	v_fma_f32 v20, v20, v60, v68
	v_fma_f32 v21, v21, v61, v69
	v_fma_f32 v23, v23, v62, v70
	v_fma_f32 v26, v26, v63, v71
	v_div_fixup_f32 v8, v8, v48, v32
	v_div_fixup_f32 v9, v9, v49, v33
	v_div_fixup_f32 v18, v18, v50, v34
	v_div_fixup_f32 v19, v19, v51, v35
	v_div_fixup_f32 v20, v20, v52, v36
	v_div_fixup_f32 v21, v21, v53, v37
	v_div_fixup_f32 v23, v23, v54, v38
	v_div_fixup_f32 v26, v26, v55, v39
	v_mul_f32_e32 v10, v10, v8
	v_mul_f32_e32 v11, v11, v9
	v_mul_f32_e32 v12, v12, v18
	v_mul_f32_e32 v13, v13, v19
	v_mul_f32_e32 v14, v14, v20
	v_mul_f32_e32 v15, v15, v21
	v_mul_f32_e32 v16, v16, v23
	v_mul_f32_e32 v17, v17, v26
	v_mul_f32_e32 v10, 0x41800000, v10
	v_mul_f32_e32 v11, 0x41800000, v11
	v_mul_f32_e32 v12, 0x41800000, v12
	v_mul_f32_e32 v13, 0x41800000, v13
	v_mul_f32_e32 v14, 0x41800000, v14
	v_mul_f32_e32 v15, 0x41800000, v15
	v_mul_f32_e32 v16, 0x41800000, v16
	v_mul_f32_e32 v17, 0x41800000, v17
	v_med3_f32 v10, v10, s91, v231
	v_med3_f32 v11, v11, s91, v231
	v_med3_f32 v12, v12, s91, v231
	v_med3_f32 v13, v13, s91, v231
	v_med3_f32 v14, v14, s91, v231
	v_med3_f32 v15, v15, s91, v231
	v_med3_f32 v16, v16, s91, v231
	v_med3_f32 v17, v17, s91, v231
	v_cvt_pk_fp8_f32 v24, v10, v11
	v_cvt_pk_fp8_f32 v25, v14, v15
	s_nop 0
	v_cvt_pk_fp8_f32 v24, v12, v13 op_sel:[0,0,1]
	v_cvt_pk_fp8_f32 v25, v16, v17 op_sel:[0,0,1]
	s_nop 0
	global_store_dwordx2 v5, v[24:25], s[42:43]
	v_add_u32_e32 v5, 0x4000, v5
	s_waitcnt vmcnt(2) lgkmcnt(0)
	v_lshlrev_b32_e32 v10, 16, v0
	v_and_b32_e32 v11, 0xffff0000, v0
	v_lshlrev_b32_e32 v12, 16, v1
	v_and_b32_e32 v13, 0xffff0000, v1
	v_lshlrev_b32_e32 v14, 16, v2
	v_and_b32_e32 v15, 0xffff0000, v2
	v_lshlrev_b32_e32 v16, 16, v3
	v_and_b32_e32 v17, 0xffff0000, v3
	v_cvt_pk_f32_fp8_e32 v[32:33], v6
	v_cvt_pk_f32_fp8_sdwa v[34:35], v6 src0_sel:WORD_1
	v_cvt_pk_f32_fp8_e32 v[36:37], v7
	v_cvt_pk_f32_fp8_sdwa v[38:39], v7 src0_sel:WORD_1
	ds_read_b128 v[0:3], v4
	v_add_u32_e32 v4, 0x2000, v4
	s_cmp_eq_u32 s44, 1
	s_cbranch_scc1 .Ldloop1b
	global_load_dwordx2 v[6:7], v22, s[40:41]
	v_add_u32_e32 v22, 0x4000, v22
; #define LAS __attribute__((address_space(3)))
; __device__ __forceinline__ float sigmoidf_(float x) { return 1.f / (1.f + __expf(-x)); }
; __device__ __forceinline__ float siluf_(float x) { return x / (1.f + __expf(-x)); }
; template <int DK, int DV, bool MLSTM>
; __device__ __forceinline__ void out_unit2(LAS unsigned char* lds, LAS unsigned char* ldstab, const OutArgs a, const int wv) {
;     ...
; #pragma unroll 1
;     for (int id = tid; id < 128 * CPR; id += 512) { const int row = id / CPR, ch = id % CPR;
;         const u32x4 y = *(const LAS u32x4*)(lds + row * TP + ch * 16);
;         const f32x4 g0 = *(const f32x4*)(a.gain + 8 * ch), g1 = *(const f32x4*)(a.gain + 8 * ch + 4);
;         float yv[8] = {bf_lo(y.x), bf_hi(y.x), bf_lo(y.y), bf_hi(y.y), bf_lo(y.z), bf_hi(y.z), bf_lo(y.w), bf_hi(y.w)};
;         float gv[8];
;         if (MLSTM) { const u32x4 g = *(const u32x4*)(a.G + (size_t)row * a.ldg + 8 * ch);
;             gv[0] = bf_lo(g.x); gv[1] = bf_hi(g.x); gv[2] = bf_lo(g.y); gv[3] = bf_hi(g.y); gv[4] = bf_lo(g.z); gv[5] = bf_hi(g.z); gv[6] = bf_lo(g.w); gv[7] = bf_hi(g.w); }
;         else { const u32x2 g = *(const u32x2*)(a.G8 + (size_t)row * a.ldg8 + 8 * ch);
;             const f32x2 e0 = __builtin_amdgcn_cvt_pk_f32_fp8((int)g.x, false), e1 = __builtin_amdgcn_cvt_pk_f32_fp8((int)g.x, true), e2 = __builtin_amdgcn_cvt_pk_f32_fp8((int)g.y, false), e3 = __builtin_amdgcn_cvt_pk_f32_fp8((int)g.y, true);
;             gv[0] = e0[0] * a.g8inv; gv[1] = e0[1] * a.g8inv; gv[2] = e1[0] * a.g8inv; gv[3] = e1[1] * a.g8inv; gv[4] = e2[0] * a.g8inv; gv[5] = e2[1] * a.g8inv; gv[6] = e3[0] * a.g8inv; gv[7] = e3[1] * a.g8inv; }
;         float gn[8] = {g0[0], g0[1], g0[2], g0[3], g1[0], g1[1], g1[2], g1[3]};
;         float ov[8];
; #pragma unroll
;         for (int i = 0; i < 8; ++i) ov[i] = yv[i] * gn[i] * (MLSTM ? sigmoidf_(gv[i]) : siluf_(gv[i]));
;         u32x2 w; w.x = pg8::pk4_fp8c(ov[0] * a.oscale, ov[1] * a.oscale, ov[2] * a.oscale, ov[3] * a.oscale); w.y = pg8::pk4_fp8c(ov[4] * a.oscale, ov[5] * a.oscale, ov[6] * a.oscale, ov[7] * a.oscale);
;         *(u32x2*)(a.Out + (size_t)row * a.ldo + 8 * ch) = w; }
.Ldloop1b:
	v_pk_mul_f32 v[10:11], v[40:41], v[10:11]
	v_pk_mul_f32 v[12:13], v[42:43], v[12:13]
	v_pk_mul_f32 v[14:15], v[44:45], v[14:15]
	v_pk_mul_f32 v[16:17], v[46:47], v[16:17]
	v_pk_mul_f32 v[32:33], v[32:33], v[162:163]
	v_pk_mul_f32 v[34:35], v[34:35], v[162:163]
	v_pk_mul_f32 v[36:37], v[36:37], v[162:163]
	v_pk_mul_f32 v[38:39], v[38:39], v[162:163]
	v_mul_f32_e32 v48, 0xbfb8aa3b, v32
	v_mul_f32_e32 v49, 0xbfb8aa3b, v33
	v_mul_f32_e32 v50, 0xbfb8aa3b, v34
	v_mul_f32_e32 v51, 0xbfb8aa3b, v35
	v_mul_f32_e32 v52, 0xbfb8aa3b, v36
	v_mul_f32_e32 v53, 0xbfb8aa3b, v37
	v_mul_f32_e32 v54, 0xbfb8aa3b, v38
	v_mul_f32_e32 v55, 0xbfb8aa3b, v39
	v_exp_f32_e32 v48, v48
	v_exp_f32_e32 v49, v49
	v_exp_f32_e32 v50, v50
	v_exp_f32_e32 v51, v51
	v_exp_f32_e32 v52, v52
	v_exp_f32_e32 v53, v53
	v_exp_f32_e32 v54, v54
	v_exp_f32_e32 v55, v55
	v_add_f32_e32 v48, 1.0, v48
	v_add_f32_e32 v49, 1.0, v49
	v_add_f32_e32 v50, 1.0, v50
	v_add_f32_e32 v51, 1.0, v51
	v_add_f32_e32 v52, 1.0, v52
	v_add_f32_e32 v53, 1.0, v53
	v_add_f32_e32 v54, 1.0, v54
	v_add_f32_e32 v55, 1.0, v55
	v_rcp_f32_e32 v56, v48
	v_rcp_f32_e32 v57, v49
	v_rcp_f32_e32 v58, v50
	v_rcp_f32_e32 v59, v51
	v_rcp_f32_e32 v60, v52
	v_rcp_f32_e32 v61, v53
	v_rcp_f32_e32 v62, v54
	v_rcp_f32_e32 v63, v55
	v_fma_f32 v8, -v48, v56, 1.0
	v_fma_f32 v9, -v49, v57, 1.0
	v_fma_f32 v18, -v50, v58, 1.0
	v_fma_f32 v19, -v51, v59, 1.0
	v_fma_f32 v20, -v52, v60, 1.0
	v_fma_f32 v21, -v53, v61, 1.0
	v_fma_f32 v23, -v54, v62, 1.0
	v_fma_f32 v26, -v55, v63, 1.0
	v_fmac_f32_e32 v56, v8, v56
	v_fmac_f32_e32 v57, v9, v57
	v_fmac_f32_e32 v58, v18, v58
	v_fmac_f32_e32 v59, v19, v59
	v_fmac_f32_e32 v60, v20, v60
	v_fmac_f32_e32 v61, v21, v61
	v_fmac_f32_e32 v62, v23, v62
	v_fmac_f32_e32 v63, v26, v63
	v_mul_f32_e32 v64, v32, v56
	v_mul_f32_e32 v65, v33, v57
	v_mul_f32_e32 v66, v34, v58
	v_mul_f32_e32 v67, v35, v59
	v_mul_f32_e32 v68, v36, v60
	v_mul_f32_e32 v69, v37, v61
	v_mul_f32_e32 v70, v38, v62
	v_mul_f32_e32 v71, v39, v63
	v_fma_f32 v8, -v48, v64, v32
	v_fma_f32 v9, -v49, v65, v33
	v_fma_f32 v18, -v50, v66, v34
	v_fma_f32 v19, -v51, v67, v35
	v_fma_f32 v20, -v52, v68, v36
	v_fma_f32 v21, -v53, v69, v37
	v_fma_f32 v23, -v54, v70, v38
	v_fma_f32 v26, -v55, v71, v39
	v_fmac_f32_e32 v64, v8, v56
	v_fmac_f32_e32 v65, v9, v57
	v_fmac_f32_e32 v66, v18, v58
	v_fmac_f32_e32 v67, v19, v59
	v_fmac_f32_e32 v68, v20, v60
	v_fmac_f32_e32 v69, v21, v61
	v_fmac_f32_e32 v70, v23, v62
	v_fmac_f32_e32 v71, v26, v63
	v_fma_f32 v8, -v48, v64, v32
	v_fma_f32 v9, -v49, v65, v33
	v_fma_f32 v18, -v50, v66, v34
	v_fma_f32 v19, -v51, v67, v35
	v_fma_f32 v20, -v52, v68, v36
	v_fma_f32 v21, -v53, v69, v37
	v_fma_f32 v23, -v54, v70, v38
	v_fma_f32 v26, -v55, v71, v39
	v_fma_f32 v8, v8, v56, v64
	v_fma_f32 v9, v9, v57, v65
	v_fma_f32 v18, v18, v58, v66
	v_fma_f32 v19, v19, v59, v67
	v_fma_f32 v20, v20, v60, v68
	v_fma_f32 v21, v21, v61, v69
	v_fma_f32 v23, v23, v62, v70
	v_fma_f32 v26, v26, v63, v71
	v_div_fixup_f32 v8, v8, v48, v32
	v_div_fixup_f32 v9, v9, v49, v33
	v_div_fixup_f32 v18, v18, v50, v34
	v_div_fixup_f32 v19, v19, v51, v35
	v_div_fixup_f32 v20, v20, v52, v36
	v_div_fixup_f32 v21, v21, v53, v37
	v_div_fixup_f32 v23, v23, v54, v38
	v_div_fixup_f32 v26, v26, v55, v39
	v_mul_f32_e32 v10, v10, v8
	v_mul_f32_e32 v11, v11, v9
	v_mul_f32_e32 v12, v12, v18
	v_mul_f32_e32 v13, v13, v19
	v_mul_f32_e32 v14, v14, v20
	v_mul_f32_e32 v15, v15, v21
	v_mul_f32_e32 v16, v16, v23
	v_mul_f32_e32 v17, v17, v26
	v_mul_f32_e32 v10, 0x41800000, v10
	v_mul_f32_e32 v11, 0x41800000, v11
	v_mul_f32_e32 v12, 0x41800000, v12
	v_mul_f32_e32 v13, 0x41800000, v13
	v_mul_f32_e32 v14, 0x41800000, v14
	v_mul_f32_e32 v15, 0x41800000, v15
	v_mul_f32_e32 v16, 0x41800000, v16
	v_mul_f32_e32 v17, 0x41800000, v17
	v_med3_f32 v10, v10, s91, v231
	v_med3_f32 v11, v11, s91, v231
	v_med3_f32 v12, v12, s91, v231
	v_med3_f32 v13, v13, s91, v231
	v_med3_f32 v14, v14, s91, v231
	v_med3_f32 v15, v15, s91, v231
	v_med3_f32 v16, v16, s91, v231
	v_med3_f32 v17, v17, s91, v231
	v_cvt_pk_fp8_f32 v24, v10, v11
	v_cvt_pk_fp8_f32 v25, v14, v15
	s_nop 0
	v_cvt_pk_fp8_f32 v24, v12, v13 op_sel:[0,0,1]
	v_cvt_pk_fp8_f32 v25, v16, v17 op_sel:[0,0,1]
	s_nop 0
	global_store_dwordx2 v5, v[24:25], s[42:43]
	v_add_u32_e32 v5, 0x4000, v5
	s_add_i32 s44, s44, -1
	s_cmp_lg_u32 s44, 0
	s_cbranch_scc1 .Ldloop1
	s_waitcnt lgkmcnt(0)
	s_branch .LBB0_4301
